# p13 scan side: the 4 waves per WG that do not scan make the phase's expert weight copies during the RWKV scan (stride 512) instead of all 8 waves after it
# speedup vs baseline: 1.0045x; 1.0018x over previous
.LBB0_1356:
	s_waitcnt lgkmcnt(0)
	s_barrier
	s_branch .LBB0_1371
.Lcv0_idle:
	s_lshr_b32 s24, s87, 1
	s_and_b32 s0, s15, 1
	s_add_i32 s24, s24, s0
	s_lshr_b32 s0, s15, 2
	s_lshl_b32 s0, s0, 1
	s_add_i32 s24, s24, s0
	s_cmpk_gt_i32 s24, 0x11ff
	s_cbranch_scc1 .Lcv0_exit
	s_ashr_i32 s0, s24, 31
	s_lshr_b32 s0, s0, 23
	s_add_i32 s0, s24, s0
	s_ashr_i32 s0, s0, 9
	s_add_i32 s8, s0, 16
	s_ashr_i32 s9, s8, 31
	s_mov_b64 s[10:11], 0x32400000
	s_cmpk_lt_i32 s24, 0xfe01
	s_mov_b64 s[6:7], s[8:9]
	s_cbranch_scc1 .LBB0_1362
	s_cmp_gt_u32 s8, 21
	s_mov_b32 s1, 0
	s_cbranch_scc0 .LBB0_1360
	s_add_i32 s6, s0, -6
	s_mov_b32 s7, s1
	s_mov_b64 s[10:11], 0x36400000
	s_cbranch_execz .LBB0_1361
	s_branch .LBB0_1362

.LBB0_1362:
	v_readlane_b32 s2, v232, 41
	v_readlane_b32 s3, v232, 42
	s_ashr_i32 s3, s2, 31
	s_lshl_b64 s[12:13], s[2:3], 27
	s_add_u32 s20, s68, s12
	s_addc_u32 s21, s69, s13
	s_add_u32 s22, s70, s12
	s_addc_u32 s23, s71, s13
	s_lshl_b32 s0, s0, 9
	s_sub_i32 s0, s24, s0
	s_cmpk_gt_i32 s0, 0xff
	s_cselect_b64 s[12:13], -1, 0
	s_and_b64 s[16:17], s[12:13], exec
	s_cselect_b32 s2, 0xff00, 0
	s_add_i32 s0, s2, s0
	s_sext_i32_i16 s2, s0
	s_bfe_u32 s2, s2, 0x5001a
	s_add_i32 s2, s0, s2
	s_sext_i32_i16 s3, s2
	s_and_b32 s2, s2, 0xffe0
	s_ashr_i32 s3, s3, 5
	s_sub_i32 s0, s0, s2
	s_lshl_b32 s14, s3, 6
	s_and_b64 s[16:17], s[12:13], exec
	s_sext_i32_i16 s2, s0
	s_cselect_b32 s0, s23, s21
	s_cselect_b32 s16, s22, s20
	s_lshl_b64 s[8:9], s[8:9], 22
	s_add_u32 s16, s16, s8
	s_addc_u32 s17, s0, s9
	s_lshl_b32 s8, s2, 6
	v_lshrrev_b32_e32 v70, 4, v1
	v_or_b32_e32 v2, s8, v70
	v_or_b32_e32 v4, 60, v2
	v_ashrrev_i32_e32 v5, 31, v4
	v_or_b32_e32 v6, 56, v2
	s_lshl_b32 s0, s15, 14
	v_lshlrev_b64 v[4:5], 11, v[4:5]
	s_ashr_i32 s15, s14, 31
	s_waitcnt vmcnt(6)
	v_lshlrev_b32_e32 v69, 2, v1
	v_ashrrev_i32_e32 v7, 31, v6
	v_lshl_add_u64 v[4:5], s[16:17], 0, v[4:5]
	s_lshl_b64 s[18:19], s[14:15], 2
	v_and_b32_e32 v68, 60, v69
	v_lshlrev_b64 v[6:7], 11, v[6:7]
	v_lshl_add_u64 v[4:5], v[4:5], 0, s[18:19]
	v_mov_b32_e32 v67, 0
	v_lshlrev_b32_e32 v66, 2, v68
	v_lshl_add_u64 v[6:7], s[16:17], 0, v[6:7]
	v_lshl_add_u64 v[4:5], v[4:5], 0, v[66:67]
	v_lshl_add_u64 v[6:7], v[6:7], 0, s[18:19]
	v_lshl_add_u64 v[6:7], v[6:7], 0, v[66:67]
	global_load_dwordx4 v[10:13], v[4:5], off nt
	global_load_dwordx4 v[14:17], v[6:7], off nt
	v_or_b32_e32 v4, 52, v2
	v_ashrrev_i32_e32 v5, 31, v4
	v_or_b32_e32 v6, 48, v2
	v_lshlrev_b64 v[4:5], 11, v[4:5]
	v_ashrrev_i32_e32 v7, 31, v6
	v_lshl_add_u64 v[4:5], s[16:17], 0, v[4:5]
	v_lshlrev_b64 v[6:7], 11, v[6:7]
	v_lshl_add_u64 v[4:5], v[4:5], 0, s[18:19]
	v_lshl_add_u64 v[6:7], s[16:17], 0, v[6:7]
	v_lshl_add_u64 v[4:5], v[4:5], 0, v[66:67]
	v_lshl_add_u64 v[6:7], v[6:7], 0, s[18:19]
	v_lshl_add_u64 v[6:7], v[6:7], 0, v[66:67]
	global_load_dwordx4 v[18:21], v[4:5], off nt
	global_load_dwordx4 v[22:25], v[6:7], off nt
	v_or_b32_e32 v4, 44, v2
	v_ashrrev_i32_e32 v5, 31, v4
	v_or_b32_e32 v6, 40, v2
	v_lshlrev_b64 v[4:5], 11, v[4:5]
	v_ashrrev_i32_e32 v7, 31, v6
	v_lshl_add_u64 v[4:5], s[16:17], 0, v[4:5]
	v_lshlrev_b64 v[6:7], 11, v[6:7]
	v_lshl_add_u64 v[4:5], v[4:5], 0, s[18:19]
	v_lshl_add_u64 v[6:7], s[16:17], 0, v[6:7]
	v_lshl_add_u64 v[4:5], v[4:5], 0, v[66:67]
	v_lshl_add_u64 v[6:7], v[6:7], 0, s[18:19]
	v_lshl_add_u64 v[6:7], v[6:7], 0, v[66:67]
	global_load_dwordx4 v[62:65], v[4:5], off nt
	global_load_dwordx4 v[58:61], v[6:7], off nt
	v_or_b32_e32 v4, 36, v2
	v_ashrrev_i32_e32 v5, 31, v4
	v_or_b32_e32 v6, 32, v2
	v_lshlrev_b64 v[4:5], 11, v[4:5]
	v_ashrrev_i32_e32 v7, 31, v6
	v_lshl_add_u64 v[4:5], s[16:17], 0, v[4:5]
	v_lshlrev_b64 v[6:7], 11, v[6:7]
	v_lshl_add_u64 v[4:5], v[4:5], 0, s[18:19]
	v_lshl_add_u64 v[6:7], s[16:17], 0, v[6:7]
	v_lshl_add_u64 v[4:5], v[4:5], 0, v[66:67]
	v_lshl_add_u64 v[6:7], v[6:7], 0, s[18:19]
	v_lshl_add_u64 v[6:7], v[6:7], 0, v[66:67]
	global_load_dwordx4 v[54:57], v[4:5], off nt
	global_load_dwordx4 v[50:53], v[6:7], off nt
	v_or_b32_e32 v4, 28, v2
	v_ashrrev_i32_e32 v5, 31, v4
	v_or_b32_e32 v6, 24, v2
	v_lshlrev_b64 v[4:5], 11, v[4:5]
	v_ashrrev_i32_e32 v7, 31, v6
	v_lshl_add_u64 v[4:5], s[16:17], 0, v[4:5]
	v_lshlrev_b64 v[6:7], 11, v[6:7]
	v_lshl_add_u64 v[4:5], v[4:5], 0, s[18:19]
	v_lshl_add_u64 v[6:7], s[16:17], 0, v[6:7]
	v_lshl_add_u64 v[4:5], v[4:5], 0, v[66:67]
	v_lshl_add_u64 v[6:7], v[6:7], 0, s[18:19]
	v_lshl_add_u64 v[6:7], v[6:7], 0, v[66:67]
	global_load_dwordx4 v[46:49], v[4:5], off nt
	global_load_dwordx4 v[42:45], v[6:7], off nt
	v_or_b32_e32 v4, 20, v2
	v_ashrrev_i32_e32 v5, 31, v4
	v_or_b32_e32 v6, 16, v2
	v_lshlrev_b64 v[4:5], 11, v[4:5]
	v_ashrrev_i32_e32 v7, 31, v6
	v_lshl_add_u64 v[4:5], s[16:17], 0, v[4:5]
	v_lshlrev_b64 v[6:7], 11, v[6:7]
	v_lshl_add_u64 v[4:5], v[4:5], 0, s[18:19]
	v_lshl_add_u64 v[6:7], s[16:17], 0, v[6:7]
	v_lshl_add_u64 v[4:5], v[4:5], 0, v[66:67]
	v_lshl_add_u64 v[6:7], v[6:7], 0, s[18:19]
	v_lshl_add_u64 v[6:7], v[6:7], 0, v[66:67]
	global_load_dwordx4 v[38:41], v[4:5], off nt
	global_load_dwordx4 v[34:37], v[6:7], off nt
	v_or_b32_e32 v4, 12, v2
	v_ashrrev_i32_e32 v5, 31, v4
	v_or_b32_e32 v6, 8, v2
	v_lshlrev_b64 v[4:5], 11, v[4:5]
	v_ashrrev_i32_e32 v7, 31, v6
	v_lshl_add_u64 v[4:5], s[16:17], 0, v[4:5]
	v_lshlrev_b64 v[6:7], 11, v[6:7]
	v_lshl_add_u64 v[4:5], v[4:5], 0, s[18:19]
	v_lshl_add_u64 v[6:7], s[16:17], 0, v[6:7]
	v_lshl_add_u64 v[4:5], v[4:5], 0, v[66:67]
	v_lshl_add_u64 v[6:7], v[6:7], 0, s[18:19]
	v_lshl_add_u64 v[6:7], v[6:7], 0, v[66:67]
	global_load_dwordx4 v[30:33], v[4:5], off nt
	global_load_dwordx4 v[26:29], v[6:7], off nt
	v_or_b32_e32 v4, 4, v2
	v_ashrrev_i32_e32 v5, 31, v4
	v_ashrrev_i32_e32 v3, 31, v2
	v_lshlrev_b64 v[4:5], 11, v[4:5]
	v_lshlrev_b64 v[2:3], 11, v[2:3]
	s_add_i32 s0, s0, 0
	v_lshl_add_u64 v[4:5], s[16:17], 0, v[4:5]
	v_lshl_add_u64 v[2:3], s[16:17], 0, v[2:3]
	v_lshl_add_u64 v[4:5], v[4:5], 0, s[18:19]
	v_lshl_add_u64 v[2:3], v[2:3], 0, s[18:19]
	v_lshl_add_u32 v74, v70, 8, s0
	v_lshlrev_b32_e32 v71, 2, v70
	v_lshl_add_u64 v[4:5], v[4:5], 0, v[66:67]
	v_lshl_add_u64 v[2:3], v[2:3], 0, v[66:67]
	v_add3_u32 v71, v74, v71, v66
	v_bitop3_b32 v66, v68, v70, 1 bitop3:0x36
	v_lshl_add_u32 v72, v66, 2, v74
	v_bitop3_b32 v66, v68, v70, 2 bitop3:0x36
	v_lshl_add_u32 v73, v66, 2, v74
	v_bitop3_b32 v66, v68, v70, 3 bitop3:0x36
	v_or_b32_e32 v75, 4, v70
	v_lshl_add_u32 v74, v66, 2, v74
	v_bitop3_b32 v66, v70, v68, 4 bitop3:0x36
	v_lshl_add_u32 v79, v75, 8, s0
	v_lshl_add_u32 v76, v66, 2, v79
	v_bitop3_b32 v66, v68, v75, 1 bitop3:0x36
	v_lshl_add_u32 v77, v66, 2, v79
	v_bitop3_b32 v66, v68, v75, 2 bitop3:0x36
	v_lshl_add_u32 v78, v66, 2, v79
	v_bitop3_b32 v66, v68, v75, 3 bitop3:0x36
	v_or_b32_e32 v80, 8, v70
	v_lshl_add_u32 v79, v66, 2, v79
	v_bitop3_b32 v66, v70, v68, 8 bitop3:0x36
	v_lshl_add_u32 v84, v80, 8, s0
	v_lshl_add_u32 v81, v66, 2, v84
	v_bitop3_b32 v66, v68, v80, 1 bitop3:0x36
	v_lshl_add_u32 v82, v66, 2, v84
	v_bitop3_b32 v66, v68, v80, 2 bitop3:0x36
	global_load_dwordx4 v[6:9], v[4:5], off nt
	s_nop 0
	global_load_dwordx4 v[2:5], v[2:3], off nt
	v_lshl_add_u32 v83, v66, 2, v84
	v_bitop3_b32 v66, v68, v80, 3 bitop3:0x36
	v_or_b32_e32 v85, 12, v70
	v_lshl_add_u32 v84, v66, 2, v84
	v_bitop3_b32 v66, v70, v68, 12 bitop3:0x36
	s_waitcnt vmcnt(17)
	v_lshl_add_u32 v89, v85, 8, s0
	v_lshl_add_u32 v86, v66, 2, v89
	v_bitop3_b32 v66, v68, v85, 1 bitop3:0x36
	v_lshl_add_u32 v87, v66, 2, v89
	v_bitop3_b32 v66, v68, v85, 2 bitop3:0x36
	v_lshl_add_u32 v88, v66, 2, v89
	v_bitop3_b32 v66, v68, v85, 3 bitop3:0x36
	s_waitcnt vmcnt(16)
	v_or_b32_e32 v90, 16, v70
	v_lshl_add_u32 v89, v66, 2, v89
	v_bitop3_b32 v66, v70, v68, 16 bitop3:0x36
	v_lshl_add_u32 v94, v90, 8, s0
	v_lshl_add_u32 v91, v66, 2, v94
	v_bitop3_b32 v66, v68, v90, 1 bitop3:0x36
	v_lshl_add_u32 v92, v66, 2, v94
	v_bitop3_b32 v66, v68, v90, 2 bitop3:0x36
	v_lshl_add_u32 v93, v66, 2, v94
	v_bitop3_b32 v66, v68, v90, 3 bitop3:0x36
	v_or_b32_e32 v95, 20, v70
	v_lshl_add_u32 v94, v66, 2, v94
	v_bitop3_b32 v66, v70, v68, 20 bitop3:0x36
	v_lshl_add_u32 v99, v95, 8, s0
	v_lshl_add_u32 v96, v66, 2, v99
	v_bitop3_b32 v66, v68, v95, 1 bitop3:0x36
	v_lshl_add_u32 v97, v66, 2, v99
	v_bitop3_b32 v66, v68, v95, 2 bitop3:0x36
	v_lshl_add_u32 v98, v66, 2, v99
	v_bitop3_b32 v66, v68, v95, 3 bitop3:0x36
	v_or_b32_e32 v100, 24, v70
	v_lshl_add_u32 v99, v66, 2, v99
	v_bitop3_b32 v66, v70, v68, 24 bitop3:0x36
	v_lshl_add_u32 v104, v100, 8, s0
	v_lshl_add_u32 v101, v66, 2, v104
	v_bitop3_b32 v66, v68, v100, 1 bitop3:0x36
	v_lshl_add_u32 v102, v66, 2, v104
	v_bitop3_b32 v66, v68, v100, 2 bitop3:0x36
	v_lshl_add_u32 v103, v66, 2, v104
	v_bitop3_b32 v66, v68, v100, 3 bitop3:0x36
	v_or_b32_e32 v105, 28, v70
	v_lshl_add_u32 v104, v66, 2, v104
	v_bitop3_b32 v66, v70, v68, 28 bitop3:0x36
	v_lshl_add_u32 v109, v105, 8, s0
	v_lshl_add_u32 v106, v66, 2, v109
	v_bitop3_b32 v66, v68, v105, 1 bitop3:0x36
	v_lshl_add_u32 v107, v66, 2, v109
	v_bitop3_b32 v66, v68, v105, 2 bitop3:0x36
	v_lshl_add_u32 v108, v66, 2, v109
	v_bitop3_b32 v66, v68, v105, 3 bitop3:0x36
	v_or_b32_e32 v110, 32, v70
	v_lshl_add_u32 v109, v66, 2, v109
	v_bitop3_b32 v66, v70, v68, 32 bitop3:0x36
	v_lshl_add_u32 v114, v110, 8, s0
	v_lshl_add_u32 v111, v66, 2, v114
	v_bitop3_b32 v66, v68, v110, 1 bitop3:0x36
	v_lshl_add_u32 v112, v66, 2, v114
	v_bitop3_b32 v66, v68, v110, 2 bitop3:0x36
	v_lshl_add_u32 v113, v66, 2, v114
	v_bitop3_b32 v66, v68, v110, 3 bitop3:0x36
	v_or_b32_e32 v115, 36, v70
	v_lshl_add_u32 v114, v66, 2, v114
	v_bitop3_b32 v66, v70, v68, 36 bitop3:0x36
	v_lshl_add_u32 v119, v115, 8, s0
	v_lshl_add_u32 v116, v66, 2, v119
	v_bitop3_b32 v66, v68, v115, 1 bitop3:0x36
	v_lshl_add_u32 v117, v66, 2, v119
	v_bitop3_b32 v66, v68, v115, 2 bitop3:0x36
	v_lshl_add_u32 v118, v66, 2, v119
	v_bitop3_b32 v66, v68, v115, 3 bitop3:0x36
	v_or_b32_e32 v120, 40, v70
	v_lshl_add_u32 v119, v66, 2, v119
	v_bitop3_b32 v66, v70, v68, 40 bitop3:0x36
	v_lshl_add_u32 v124, v120, 8, s0
	v_lshl_add_u32 v121, v66, 2, v124
	v_bitop3_b32 v66, v68, v120, 1 bitop3:0x36
	v_lshl_add_u32 v122, v66, 2, v124
	v_bitop3_b32 v66, v68, v120, 2 bitop3:0x36
	v_lshl_add_u32 v123, v66, 2, v124
	v_bitop3_b32 v66, v68, v120, 3 bitop3:0x36
	v_or_b32_e32 v125, 44, v70
	v_lshl_add_u32 v124, v66, 2, v124
	v_bitop3_b32 v66, v70, v68, 44 bitop3:0x36
	v_lshl_add_u32 v129, v125, 8, s0
	v_lshl_add_u32 v126, v66, 2, v129
	v_bitop3_b32 v66, v68, v125, 1 bitop3:0x36
	v_lshl_add_u32 v127, v66, 2, v129
	v_bitop3_b32 v66, v68, v125, 2 bitop3:0x36
	v_lshl_add_u32 v128, v66, 2, v129
	v_bitop3_b32 v66, v68, v125, 3 bitop3:0x36
	v_or_b32_e32 v130, 48, v70
	v_lshl_add_u32 v129, v66, 2, v129
	v_bitop3_b32 v66, v70, v68, 48 bitop3:0x36
	v_lshl_add_u32 v134, v130, 8, s0
	v_lshl_add_u32 v131, v66, 2, v134
	v_bitop3_b32 v66, v68, v130, 1 bitop3:0x36
	v_lshl_add_u32 v132, v66, 2, v134
	v_bitop3_b32 v66, v68, v130, 2 bitop3:0x36
	v_lshl_add_u32 v133, v66, 2, v134
	v_bitop3_b32 v66, v68, v130, 3 bitop3:0x36
	v_or_b32_e32 v135, 52, v70
	v_lshl_add_u32 v134, v66, 2, v134
	v_bitop3_b32 v66, v70, v68, 52 bitop3:0x36
	v_lshl_add_u32 v139, v135, 8, s0
	v_lshl_add_u32 v136, v66, 2, v139
	v_bitop3_b32 v66, v68, v135, 1 bitop3:0x36
	v_lshl_add_u32 v137, v66, 2, v139
	v_bitop3_b32 v66, v68, v135, 2 bitop3:0x36
	v_lshl_add_u32 v138, v66, 2, v139
	v_bitop3_b32 v66, v68, v135, 3 bitop3:0x36
	v_or_b32_e32 v140, 56, v70
	v_lshl_add_u32 v139, v66, 2, v139
	v_bitop3_b32 v66, v70, v68, 56 bitop3:0x36
	v_lshl_add_u32 v144, v140, 8, s0
	v_lshl_add_u32 v141, v66, 2, v144
	v_bitop3_b32 v66, v68, v140, 1 bitop3:0x36
	v_lshl_add_u32 v142, v66, 2, v144
	v_bitop3_b32 v66, v68, v140, 2 bitop3:0x36
	v_lshl_add_u32 v143, v66, 2, v144
	v_bitop3_b32 v66, v68, v140, 3 bitop3:0x36
	v_or_b32_e32 v145, 60, v70
	v_lshl_add_u32 v144, v66, 2, v144
	v_bitop3_b32 v66, v70, v69, 60 bitop3:0x72
	v_lshl_add_u32 v69, v145, 8, s0
	v_lshl_add_u32 v146, v66, 2, v69
	v_bitop3_b32 v66, v68, v145, 1 bitop3:0x36
	v_lshl_add_u32 v147, v66, 2, v69
	v_bitop3_b32 v66, v68, v145, 2 bitop3:0x36
	v_lshl_add_u32 v148, v66, 2, v69
	v_bitop3_b32 v66, v68, v145, 3 bitop3:0x36
	v_lshl_add_u32 v149, v66, 2, v69
	v_lshlrev_b32_e32 v66, 3, v1
	v_lshrrev_b32_e32 v150, 3, v1
	v_and_b32_e32 v222, 56, v66
	v_lshl_add_u32 v69, v222, 8, s0
	v_lshlrev_b32_e32 v1, 2, v222
	v_lshlrev_b32_e32 v151, 2, v150
	v_add3_u32 v1, v69, v1, v151
	v_or_b32_e32 v151, 1, v222
	v_bitop3_b32 v152, v222, v150, 1 bitop3:0x36
	v_lshl_add_u32 v214, v151, 8, s0
	v_lshl_add_u32 v151, v152, 2, v214
	v_or_b32_e32 v152, 2, v222
	v_bitop3_b32 v153, v222, v150, 2 bitop3:0x36
	v_lshl_add_u32 v215, v152, 8, s0
	v_lshl_add_u32 v152, v153, 2, v215
	v_or_b32_e32 v153, 3, v222
	v_bitop3_b32 v154, v222, v150, 3 bitop3:0x36
	v_lshl_add_u32 v216, v153, 8, s0
	v_lshl_add_u32 v153, v154, 2, v216
	v_or_b32_e32 v154, 4, v222
	v_bitop3_b32 v155, v222, v150, 4 bitop3:0x36
	v_lshl_add_u32 v217, v154, 8, s0
	v_lshl_add_u32 v154, v155, 2, v217
	v_or_b32_e32 v155, 5, v222
	v_bitop3_b32 v156, v222, v150, 5 bitop3:0x36
	v_lshl_add_u32 v218, v155, 8, s0
	v_lshl_add_u32 v155, v156, 2, v218
	v_or_b32_e32 v156, 6, v222
	v_bitop3_b32 v157, v222, v150, 6 bitop3:0x36
	v_lshl_add_u32 v219, v156, 8, s0
	v_lshl_add_u32 v156, v157, 2, v219
	v_or_b32_e32 v157, 7, v222
	v_bitop3_b32 v158, v222, v150, 7 bitop3:0x36
	v_lshl_add_u32 v220, v157, 8, s0
	v_lshl_add_u32 v157, v158, 2, v220
	v_or_b32_e32 v158, 8, v150
	v_or_b32_e32 v167, 16, v150
	v_or_b32_e32 v176, 24, v150
	v_or_b32_e32 v185, 32, v150
	v_or_b32_e32 v194, 40, v150
	v_or_b32_e32 v203, 48, v150
	s_and_b32 s2, s14, 64
	v_bitop3_b32 v159, v66, v158, 56 bitop3:0x6c
	v_bitop3_b32 v168, v66, v167, 56 bitop3:0x6c
	v_bitop3_b32 v177, v66, v176, 56 bitop3:0x6c
	v_bitop3_b32 v186, v66, v185, 56 bitop3:0x6c
	v_bitop3_b32 v195, v66, v194, 56 bitop3:0x6c
	v_bitop3_b32 v204, v66, v203, 56 bitop3:0x6c
	v_or_b32_e32 v212, 56, v150
	v_bitop3_b32 v66, v66, v150, 56 bitop3:0x4e
	s_and_b64 s[12:13], s[12:13], exec
	v_bitop3_b32 v160, v222, v158, 1 bitop3:0x36
	v_bitop3_b32 v169, v222, v167, 1 bitop3:0x36
	v_bitop3_b32 v178, v222, v176, 1 bitop3:0x36
	v_bitop3_b32 v187, v222, v185, 1 bitop3:0x36
	v_bitop3_b32 v196, v222, v194, 1 bitop3:0x36
	v_bitop3_b32 v205, v222, v203, 1 bitop3:0x36
	v_lshl_add_u32 v213, v66, 2, v69
	v_bitop3_b32 v66, v222, v212, 1 bitop3:0x36
	s_cselect_b32 s9, 0x80, 0
	s_lshl_b32 s3, s3, 7
	v_lshl_add_u32 v160, v160, 2, v214
	v_bitop3_b32 v161, v222, v158, 2 bitop3:0x36
	v_lshl_add_u32 v169, v169, 2, v214
	v_bitop3_b32 v170, v222, v167, 2 bitop3:0x36
	v_lshl_add_u32 v178, v178, 2, v214
	v_bitop3_b32 v179, v222, v176, 2 bitop3:0x36
	v_lshl_add_u32 v187, v187, 2, v214
	v_bitop3_b32 v188, v222, v185, 2 bitop3:0x36
	v_lshl_add_u32 v196, v196, 2, v214
	v_bitop3_b32 v197, v222, v194, 2 bitop3:0x36
	v_lshl_add_u32 v205, v205, 2, v214
	v_bitop3_b32 v206, v222, v203, 2 bitop3:0x36
	v_lshl_add_u32 v214, v66, 2, v214
	v_bitop3_b32 v66, v222, v212, 2 bitop3:0x36
	s_or_b32 s2, s2, s9
	s_and_b32 s3, s3, 0xffffff00
	v_lshl_add_u32 v161, v161, 2, v215
	v_bitop3_b32 v162, v222, v158, 3 bitop3:0x36
	v_lshl_add_u32 v170, v170, 2, v215
	v_bitop3_b32 v171, v222, v167, 3 bitop3:0x36
	v_lshl_add_u32 v179, v179, 2, v215
	v_bitop3_b32 v180, v222, v176, 3 bitop3:0x36
	v_lshl_add_u32 v188, v188, 2, v215
	v_bitop3_b32 v189, v222, v185, 3 bitop3:0x36
	v_lshl_add_u32 v197, v197, 2, v215
	v_bitop3_b32 v198, v222, v194, 3 bitop3:0x36
	v_lshl_add_u32 v206, v206, 2, v215
	v_bitop3_b32 v207, v222, v203, 3 bitop3:0x36
	v_lshl_add_u32 v215, v66, 2, v215
	v_bitop3_b32 v66, v222, v212, 3 bitop3:0x36
	s_or_b32 s18, s2, s3
	s_lshl_b64 s[6:7], s[6:7], 22
	v_lshl_add_u32 v162, v162, 2, v216
	v_bitop3_b32 v163, v222, v158, 4 bitop3:0x36
	v_lshl_add_u32 v171, v171, 2, v216
	v_bitop3_b32 v172, v222, v167, 4 bitop3:0x36
	v_lshl_add_u32 v180, v180, 2, v216
	v_bitop3_b32 v181, v222, v176, 4 bitop3:0x36
	v_lshl_add_u32 v189, v189, 2, v216
	v_bitop3_b32 v190, v222, v185, 4 bitop3:0x36
	v_lshl_add_u32 v198, v198, 2, v216
	v_bitop3_b32 v199, v222, v194, 4 bitop3:0x36
	v_lshl_add_u32 v207, v207, 2, v216
	v_bitop3_b32 v208, v222, v203, 4 bitop3:0x36
	v_lshl_add_u32 v216, v66, 2, v216
	v_bitop3_b32 v66, v222, v212, 4 bitop3:0x36
	s_add_u32 s2, s4, s6
	v_lshl_add_u32 v163, v163, 2, v217
	v_bitop3_b32 v164, v222, v158, 5 bitop3:0x36
	v_lshl_add_u32 v172, v172, 2, v217
	v_bitop3_b32 v173, v222, v167, 5 bitop3:0x36
	v_lshl_add_u32 v181, v181, 2, v217
	v_bitop3_b32 v182, v222, v176, 5 bitop3:0x36
	v_lshl_add_u32 v190, v190, 2, v217
	v_bitop3_b32 v191, v222, v185, 5 bitop3:0x36
	v_lshl_add_u32 v199, v199, 2, v217
	v_bitop3_b32 v200, v222, v194, 5 bitop3:0x36
	v_lshl_add_u32 v208, v208, 2, v217
	v_bitop3_b32 v209, v222, v203, 5 bitop3:0x36
	v_lshl_add_u32 v217, v66, 2, v217
	v_bitop3_b32 v66, v222, v212, 5 bitop3:0x36
	s_addc_u32 s3, s5, s7
	v_lshl_add_u32 v164, v164, 2, v218
	v_bitop3_b32 v165, v222, v158, 6 bitop3:0x36
	v_lshl_add_u32 v173, v173, 2, v218
	v_bitop3_b32 v174, v222, v167, 6 bitop3:0x36
	v_lshl_add_u32 v182, v182, 2, v218
	v_bitop3_b32 v183, v222, v176, 6 bitop3:0x36
	v_lshl_add_u32 v191, v191, 2, v218
	v_bitop3_b32 v192, v222, v185, 6 bitop3:0x36
	v_lshl_add_u32 v200, v200, 2, v218
	v_bitop3_b32 v201, v222, v194, 6 bitop3:0x36
	v_lshl_add_u32 v209, v209, 2, v218
	v_bitop3_b32 v210, v222, v203, 6 bitop3:0x36
	v_lshl_add_u32 v218, v66, 2, v218
	v_bitop3_b32 v66, v222, v212, 6 bitop3:0x36
	s_add_u32 s6, s2, s10
	v_lshl_add_u32 v165, v165, 2, v219
	v_bitop3_b32 v166, v222, v158, 7 bitop3:0x36
	v_lshl_add_u32 v174, v174, 2, v219
	v_bitop3_b32 v175, v222, v167, 7 bitop3:0x36
	v_lshl_add_u32 v183, v183, 2, v219
	v_bitop3_b32 v184, v222, v176, 7 bitop3:0x36
	v_lshl_add_u32 v192, v192, 2, v219
	v_bitop3_b32 v193, v222, v185, 7 bitop3:0x36
	v_lshl_add_u32 v201, v201, 2, v219
	v_bitop3_b32 v202, v222, v194, 7 bitop3:0x36
	v_lshl_add_u32 v210, v210, 2, v219
	v_bitop3_b32 v211, v222, v203, 7 bitop3:0x36
	v_lshl_add_u32 v219, v66, 2, v219
	v_bitop3_b32 v66, v222, v212, 7 bitop3:0x36
	s_mov_b32 s1, 0
	s_addc_u32 s7, s3, s11
	v_lshl_add_u32 v159, v159, 2, v69
	v_lshl_add_u32 v166, v166, 2, v220
	v_lshl_add_u32 v168, v168, 2, v69
	v_lshl_add_u32 v175, v175, 2, v220
	v_lshl_add_u32 v177, v177, 2, v69
	v_lshl_add_u32 v184, v184, 2, v220
	v_lshl_add_u32 v186, v186, 2, v69
	v_lshl_add_u32 v193, v193, 2, v220
	v_lshl_add_u32 v195, v195, 2, v69
	v_lshl_add_u32 v202, v202, 2, v220
	v_lshl_add_u32 v204, v204, 2, v69
	v_lshl_add_u32 v211, v211, 2, v220
	v_lshl_add_u32 v220, v66, 2, v220
	s_add_i32 s19, s24, 0x200
	v_lshlrev_b32_e32 v66, 2, v68
	s_movk_i32 s24, 0x7fff
	s_mov_b32 s25, 0xffff0000
	v_lshlrev_b32_e32 v68, 1, v222
	s_branch .LBB0_1365

.LBB0_1364:
	ds_read_b32 v69, v1
	ds_read_b32 v221, v151
	ds_read_b32 v223, v152
	ds_read_b32 v224, v153
	ds_read_b32 v225, v154
	ds_read_b32 v226, v155
	ds_read_b32 v227, v156
	ds_read_b32 v228, v157
	s_waitcnt lgkmcnt(7)
	v_bfe_u32 v222, v69, 16, 1
	v_add3_u32 v69, v69, v222, s24
	s_waitcnt lgkmcnt(6)
	v_bfe_u32 v222, v221, 16, 1
	v_lshrrev_b32_e32 v69, 16, v69
	v_add3_u32 v221, v221, v222, s24
	v_and_or_b32 v222, v221, s25, v69
	s_waitcnt lgkmcnt(5)
	v_bfe_u32 v69, v223, 16, 1
	v_add3_u32 v69, v223, v69, s24
	s_waitcnt lgkmcnt(4)
	v_bfe_u32 v221, v224, 16, 1
	v_lshrrev_b32_e32 v69, 16, v69
	v_add3_u32 v221, v224, v221, s24
	v_and_or_b32 v223, v221, s25, v69
	s_waitcnt lgkmcnt(3)
	v_bfe_u32 v69, v225, 16, 1
	v_add3_u32 v69, v225, v69, s24
	s_waitcnt lgkmcnt(2)
	v_bfe_u32 v221, v226, 16, 1
	v_lshrrev_b32_e32 v69, 16, v69
	v_add3_u32 v221, v226, v221, s24
	v_and_or_b32 v224, v221, s25, v69
	s_waitcnt lgkmcnt(1)
	v_bfe_u32 v69, v227, 16, 1
	v_add_u32_e32 v226, s18, v150
	v_add3_u32 v69, v227, v69, s24
	v_ashrrev_i32_e32 v227, 31, v226
	s_waitcnt lgkmcnt(0)
	v_bfe_u32 v221, v228, 16, 1
	v_lshlrev_b64 v[226:227], 12, v[226:227]
	s_ashr_i32 s9, s8, 31
	v_lshrrev_b32_e32 v69, 16, v69
	v_add3_u32 v221, v228, v221, s24
	v_lshl_add_u64 v[226:227], s[6:7], 0, v[226:227]
	s_lshl_b64 s[8:9], s[8:9], 1
	v_and_or_b32 v225, v221, s25, v69
	v_lshl_add_u64 v[226:227], v[226:227], 0, s[8:9]
	v_mov_b32_e32 v69, v67
	v_lshl_add_u64 v[226:227], v[226:227], 0, v[68:69]
	global_store_dwordx4 v[226:227], v[222:225], off nt
	ds_read_b32 v221, v159
	ds_read_b32 v222, v160
	ds_read_b32 v223, v161
	ds_read_b32 v224, v162
	ds_read_b32 v225, v163
	ds_read_b32 v226, v164
	ds_read_b32 v227, v165
	ds_read_b32 v228, v166
	s_waitcnt lgkmcnt(7)
	v_bfe_u32 v229, v221, 16, 1
	v_add3_u32 v221, v221, v229, s24
	s_waitcnt lgkmcnt(6)
	v_bfe_u32 v229, v222, 16, 1
	v_lshrrev_b32_e32 v221, 16, v221
	v_add3_u32 v222, v222, v229, s24
	v_and_or_b32 v222, v222, s25, v221
	s_waitcnt lgkmcnt(5)
	v_bfe_u32 v221, v223, 16, 1
	v_add3_u32 v221, v223, v221, s24
	s_waitcnt lgkmcnt(4)
	v_bfe_u32 v223, v224, 16, 1
	v_lshrrev_b32_e32 v221, 16, v221
	v_add3_u32 v223, v224, v223, s24
	v_and_or_b32 v223, v223, s25, v221
	s_waitcnt lgkmcnt(3)
	v_bfe_u32 v221, v225, 16, 1
	v_add3_u32 v221, v225, v221, s24
	s_waitcnt lgkmcnt(2)
	v_bfe_u32 v224, v226, 16, 1
	v_lshrrev_b32_e32 v221, 16, v221
	v_add3_u32 v224, v226, v224, s24
	v_and_or_b32 v224, v224, s25, v221
	s_waitcnt lgkmcnt(1)
	v_bfe_u32 v221, v227, 16, 1
	v_add_u32_e32 v226, s18, v158
	v_add3_u32 v221, v227, v221, s24
	v_ashrrev_i32_e32 v227, 31, v226
	v_lshlrev_b64 v[226:227], 12, v[226:227]
	s_waitcnt lgkmcnt(0)
	v_bfe_u32 v225, v228, 16, 1
	v_lshl_add_u64 v[226:227], s[6:7], 0, v[226:227]
	v_lshrrev_b32_e32 v221, 16, v221
	v_add3_u32 v225, v228, v225, s24
	v_lshl_add_u64 v[226:227], v[226:227], 0, s[8:9]
	v_and_or_b32 v225, v225, s25, v221
	v_lshl_add_u64 v[226:227], v[226:227], 0, v[68:69]
	global_store_dwordx4 v[226:227], v[222:225], off nt
	ds_read_b32 v221, v168
	ds_read_b32 v222, v169
	ds_read_b32 v223, v170
	ds_read_b32 v224, v171
	ds_read_b32 v225, v172
	ds_read_b32 v226, v173
	ds_read_b32 v227, v174
	ds_read_b32 v228, v175
	s_waitcnt lgkmcnt(7)
	v_bfe_u32 v229, v221, 16, 1
	v_add3_u32 v221, v221, v229, s24
	s_waitcnt lgkmcnt(6)
	v_bfe_u32 v229, v222, 16, 1
	v_lshrrev_b32_e32 v221, 16, v221
	v_add3_u32 v222, v222, v229, s24
	v_and_or_b32 v222, v222, s25, v221
	s_waitcnt lgkmcnt(5)
	v_bfe_u32 v221, v223, 16, 1
	v_add3_u32 v221, v223, v221, s24
	s_waitcnt lgkmcnt(4)
	v_bfe_u32 v223, v224, 16, 1
	v_lshrrev_b32_e32 v221, 16, v221
	v_add3_u32 v223, v224, v223, s24
	v_and_or_b32 v223, v223, s25, v221
	s_waitcnt lgkmcnt(3)
	v_bfe_u32 v221, v225, 16, 1
	v_add3_u32 v221, v225, v221, s24
	s_waitcnt lgkmcnt(2)
	v_bfe_u32 v224, v226, 16, 1
	v_lshrrev_b32_e32 v221, 16, v221
	v_add3_u32 v224, v226, v224, s24
	v_and_or_b32 v224, v224, s25, v221
	s_waitcnt lgkmcnt(1)
	v_bfe_u32 v221, v227, 16, 1
	v_add_u32_e32 v226, s18, v167
	v_add3_u32 v221, v227, v221, s24
	v_ashrrev_i32_e32 v227, 31, v226
	v_lshlrev_b64 v[226:227], 12, v[226:227]
	s_waitcnt lgkmcnt(0)
	v_bfe_u32 v225, v228, 16, 1
	v_lshl_add_u64 v[226:227], s[6:7], 0, v[226:227]
	v_lshrrev_b32_e32 v221, 16, v221
	v_add3_u32 v225, v228, v225, s24
	v_lshl_add_u64 v[226:227], v[226:227], 0, s[8:9]
	v_and_or_b32 v225, v225, s25, v221
	v_lshl_add_u64 v[226:227], v[226:227], 0, v[68:69]
	global_store_dwordx4 v[226:227], v[222:225], off nt
	ds_read_b32 v221, v177
	ds_read_b32 v222, v178
	ds_read_b32 v223, v179
	ds_read_b32 v224, v180
	ds_read_b32 v225, v181
	ds_read_b32 v226, v182
	ds_read_b32 v227, v183
	ds_read_b32 v228, v184
	s_waitcnt lgkmcnt(7)
	v_bfe_u32 v229, v221, 16, 1
	v_add3_u32 v221, v221, v229, s24
	s_waitcnt lgkmcnt(6)
	v_bfe_u32 v229, v222, 16, 1
	v_lshrrev_b32_e32 v221, 16, v221
	v_add3_u32 v222, v222, v229, s24
	v_and_or_b32 v222, v222, s25, v221
	s_waitcnt lgkmcnt(5)
	v_bfe_u32 v221, v223, 16, 1
	v_add3_u32 v221, v223, v221, s24
	s_waitcnt lgkmcnt(4)
	v_bfe_u32 v223, v224, 16, 1
	v_lshrrev_b32_e32 v221, 16, v221
	v_add3_u32 v223, v224, v223, s24
	v_and_or_b32 v223, v223, s25, v221
	s_waitcnt lgkmcnt(3)
	v_bfe_u32 v221, v225, 16, 1
	v_add3_u32 v221, v225, v221, s24
	s_waitcnt lgkmcnt(2)
	v_bfe_u32 v224, v226, 16, 1
	v_lshrrev_b32_e32 v221, 16, v221
	v_add3_u32 v224, v226, v224, s24
	v_and_or_b32 v224, v224, s25, v221
	s_waitcnt lgkmcnt(1)
	v_bfe_u32 v221, v227, 16, 1
	v_add_u32_e32 v226, s18, v176
	v_add3_u32 v221, v227, v221, s24
	v_ashrrev_i32_e32 v227, 31, v226
	v_lshlrev_b64 v[226:227], 12, v[226:227]
	s_waitcnt lgkmcnt(0)
	v_bfe_u32 v225, v228, 16, 1
	v_lshl_add_u64 v[226:227], s[6:7], 0, v[226:227]
	v_lshrrev_b32_e32 v221, 16, v221
	v_add3_u32 v225, v228, v225, s24
	v_lshl_add_u64 v[226:227], v[226:227], 0, s[8:9]
	v_and_or_b32 v225, v225, s25, v221
	v_lshl_add_u64 v[226:227], v[226:227], 0, v[68:69]
	global_store_dwordx4 v[226:227], v[222:225], off nt
	ds_read_b32 v221, v186
	ds_read_b32 v222, v187
	ds_read_b32 v223, v188
	ds_read_b32 v224, v189
	ds_read_b32 v225, v190
	ds_read_b32 v226, v191
	ds_read_b32 v227, v192
	ds_read_b32 v228, v193
	s_waitcnt lgkmcnt(7)
	v_bfe_u32 v229, v221, 16, 1
	v_add3_u32 v221, v221, v229, s24
	s_waitcnt lgkmcnt(6)
	v_bfe_u32 v229, v222, 16, 1
	v_lshrrev_b32_e32 v221, 16, v221
	v_add3_u32 v222, v222, v229, s24
	v_and_or_b32 v222, v222, s25, v221
	s_waitcnt lgkmcnt(5)
	v_bfe_u32 v221, v223, 16, 1
	v_add3_u32 v221, v223, v221, s24
	s_waitcnt lgkmcnt(4)
	v_bfe_u32 v223, v224, 16, 1
	v_lshrrev_b32_e32 v221, 16, v221
	v_add3_u32 v223, v224, v223, s24
	v_and_or_b32 v223, v223, s25, v221
	s_waitcnt lgkmcnt(3)
	v_bfe_u32 v221, v225, 16, 1
	v_add3_u32 v221, v225, v221, s24
	s_waitcnt lgkmcnt(2)
	v_bfe_u32 v224, v226, 16, 1
	v_lshrrev_b32_e32 v221, 16, v221
	v_add3_u32 v224, v226, v224, s24
	v_and_or_b32 v224, v224, s25, v221
	s_waitcnt lgkmcnt(1)
	v_bfe_u32 v221, v227, 16, 1
	v_add_u32_e32 v226, s18, v185
	v_add3_u32 v221, v227, v221, s24
	v_ashrrev_i32_e32 v227, 31, v226
	v_lshlrev_b64 v[226:227], 12, v[226:227]
	s_waitcnt lgkmcnt(0)
	v_bfe_u32 v225, v228, 16, 1
	v_lshl_add_u64 v[226:227], s[6:7], 0, v[226:227]
	v_lshrrev_b32_e32 v221, 16, v221
	v_add3_u32 v225, v228, v225, s24
	v_lshl_add_u64 v[226:227], v[226:227], 0, s[8:9]
	v_and_or_b32 v225, v225, s25, v221
	v_lshl_add_u64 v[226:227], v[226:227], 0, v[68:69]
	global_store_dwordx4 v[226:227], v[222:225], off nt
	ds_read_b32 v221, v195
	ds_read_b32 v222, v196
	ds_read_b32 v223, v197
	ds_read_b32 v224, v198
	ds_read_b32 v225, v199
	ds_read_b32 v226, v200
	ds_read_b32 v227, v201
	ds_read_b32 v228, v202
	s_waitcnt lgkmcnt(7)
	v_bfe_u32 v229, v221, 16, 1
	v_add3_u32 v221, v221, v229, s24
	s_waitcnt lgkmcnt(6)
	v_bfe_u32 v229, v222, 16, 1
	v_lshrrev_b32_e32 v221, 16, v221
	v_add3_u32 v222, v222, v229, s24
	v_and_or_b32 v222, v222, s25, v221
	s_waitcnt lgkmcnt(5)
	v_bfe_u32 v221, v223, 16, 1
	v_add3_u32 v221, v223, v221, s24
	s_waitcnt lgkmcnt(4)
	v_bfe_u32 v223, v224, 16, 1
	v_lshrrev_b32_e32 v221, 16, v221
	v_add3_u32 v223, v224, v223, s24
	v_and_or_b32 v223, v223, s25, v221
	s_waitcnt lgkmcnt(3)
	v_bfe_u32 v221, v225, 16, 1
	v_add3_u32 v221, v225, v221, s24
	s_waitcnt lgkmcnt(2)
	v_bfe_u32 v224, v226, 16, 1
	v_lshrrev_b32_e32 v221, 16, v221
	v_add3_u32 v224, v226, v224, s24
	v_and_or_b32 v224, v224, s25, v221
	s_waitcnt lgkmcnt(1)
	v_bfe_u32 v221, v227, 16, 1
	v_add_u32_e32 v226, s18, v194
	v_add3_u32 v221, v227, v221, s24
	v_ashrrev_i32_e32 v227, 31, v226
	v_lshlrev_b64 v[226:227], 12, v[226:227]
	s_waitcnt lgkmcnt(0)
	v_bfe_u32 v225, v228, 16, 1
	v_lshl_add_u64 v[226:227], s[6:7], 0, v[226:227]
	v_lshrrev_b32_e32 v221, 16, v221
	v_add3_u32 v225, v228, v225, s24
	v_lshl_add_u64 v[226:227], v[226:227], 0, s[8:9]
	v_and_or_b32 v225, v225, s25, v221
	v_lshl_add_u64 v[226:227], v[226:227], 0, v[68:69]
	global_store_dwordx4 v[226:227], v[222:225], off nt
	ds_read_b32 v221, v204
	ds_read_b32 v222, v205
	ds_read_b32 v223, v206
	ds_read_b32 v224, v207
	ds_read_b32 v225, v208
	ds_read_b32 v226, v209
	ds_read_b32 v227, v210
	ds_read_b32 v228, v211
	s_waitcnt lgkmcnt(7)
	v_bfe_u32 v229, v221, 16, 1
	v_add3_u32 v221, v221, v229, s24
	s_waitcnt lgkmcnt(6)
	v_bfe_u32 v229, v222, 16, 1
	v_lshrrev_b32_e32 v221, 16, v221
	v_add3_u32 v222, v222, v229, s24
	v_and_or_b32 v222, v222, s25, v221
	s_waitcnt lgkmcnt(5)
	v_bfe_u32 v221, v223, 16, 1
	v_add3_u32 v221, v223, v221, s24
	s_waitcnt lgkmcnt(4)
	v_bfe_u32 v223, v224, 16, 1
	v_lshrrev_b32_e32 v221, 16, v221
	v_add3_u32 v223, v224, v223, s24
	v_and_or_b32 v223, v223, s25, v221
	s_waitcnt lgkmcnt(3)
	v_bfe_u32 v221, v225, 16, 1
	v_add3_u32 v221, v225, v221, s24
	s_waitcnt lgkmcnt(2)
	v_bfe_u32 v224, v226, 16, 1
	v_lshrrev_b32_e32 v221, 16, v221
	v_add3_u32 v224, v226, v224, s24
	v_and_or_b32 v224, v224, s25, v221
	s_waitcnt lgkmcnt(1)
	v_bfe_u32 v221, v227, 16, 1
	v_add_u32_e32 v226, s18, v203
	v_add3_u32 v221, v227, v221, s24
	v_ashrrev_i32_e32 v227, 31, v226
	v_lshlrev_b64 v[226:227], 12, v[226:227]
	s_waitcnt lgkmcnt(0)
	v_bfe_u32 v225, v228, 16, 1
	v_lshl_add_u64 v[226:227], s[6:7], 0, v[226:227]
	v_lshrrev_b32_e32 v221, 16, v221
	v_add3_u32 v225, v228, v225, s24
	v_lshl_add_u64 v[226:227], v[226:227], 0, s[8:9]
	v_and_or_b32 v225, v225, s25, v221
	v_lshl_add_u64 v[226:227], v[226:227], 0, v[68:69]
	global_store_dwordx4 v[226:227], v[222:225], off nt
	ds_read_b32 v221, v213
	ds_read_b32 v222, v214
	ds_read_b32 v223, v215
	ds_read_b32 v224, v216
	ds_read_b32 v225, v217
	ds_read_b32 v226, v218
	ds_read_b32 v227, v219
	ds_read_b32 v228, v220
	s_waitcnt lgkmcnt(7)
	v_bfe_u32 v229, v221, 16, 1
	v_add3_u32 v221, v221, v229, s24
	s_waitcnt lgkmcnt(6)
	v_bfe_u32 v229, v222, 16, 1
	v_lshrrev_b32_e32 v221, 16, v221
	v_add3_u32 v222, v222, v229, s24
	v_and_or_b32 v222, v222, s25, v221
	s_waitcnt lgkmcnt(5)
	v_bfe_u32 v221, v223, 16, 1
	v_add3_u32 v221, v223, v221, s24
	s_waitcnt lgkmcnt(4)
	v_bfe_u32 v223, v224, 16, 1
	v_lshrrev_b32_e32 v221, 16, v221
	v_add3_u32 v223, v224, v223, s24
	v_and_or_b32 v223, v223, s25, v221
	s_waitcnt lgkmcnt(3)
	v_bfe_u32 v221, v225, 16, 1
	v_add3_u32 v221, v225, v221, s24
	s_waitcnt lgkmcnt(2)
	v_bfe_u32 v224, v226, 16, 1
	v_lshrrev_b32_e32 v221, 16, v221
	v_add3_u32 v224, v226, v224, s24
	v_and_or_b32 v224, v224, s25, v221
	s_waitcnt lgkmcnt(1)
	v_bfe_u32 v221, v227, 16, 1
	v_add_u32_e32 v226, s18, v212
	v_add3_u32 v221, v227, v221, s24
	v_ashrrev_i32_e32 v227, 31, v226
	v_lshlrev_b64 v[226:227], 12, v[226:227]
	s_waitcnt lgkmcnt(0)
	v_bfe_u32 v225, v228, 16, 1
	v_lshl_add_u64 v[226:227], s[6:7], 0, v[226:227]
	v_lshrrev_b32_e32 v221, 16, v221
	v_add3_u32 v225, v228, v225, s24
	v_lshl_add_u64 v[226:227], v[226:227], 0, s[8:9]
	v_and_or_b32 v225, v225, s25, v221
	v_lshl_add_u64 v[226:227], v[226:227], 0, v[68:69]
	global_store_dwordx4 v[226:227], v[222:225], off nt
	s_waitcnt lgkmcnt(0)
	s_addk_i32 s19, 0x200
	s_cmpk_gt_i32 s26, 0xfff
	s_mov_b64 s[6:7], s[10:11]
	s_mov_b32 s8, s0
	s_mov_b32 s18, s12
	s_cbranch_scc1 .Lcv0_exit
.LBB0_1365:
	s_waitcnt vmcnt(0)
	ds_write_b32 v71, v2
	ds_write_b32 v72, v3
	ds_write_b32 v73, v4
	ds_write_b32 v74, v5
	ds_write_b32 v76, v6
	ds_write_b32 v77, v7
	ds_write_b32 v78, v8
	ds_write_b32 v79, v9
	ds_write_b32 v81, v26
	ds_write_b32 v82, v27
	ds_write_b32 v83, v28
	ds_write_b32 v84, v29
	ds_write_b32 v86, v30
	ds_write_b32 v87, v31
	ds_write_b32 v88, v32
	ds_write_b32 v89, v33
	ds_write_b32 v91, v34
	ds_write_b32 v92, v35
	ds_write_b32 v93, v36
	ds_write_b32 v94, v37
	ds_write_b32 v96, v38
	ds_write_b32 v97, v39
	ds_write_b32 v98, v40
	ds_write_b32 v99, v41
	ds_write_b32 v101, v42
	ds_write_b32 v102, v43
	ds_write_b32 v103, v44
	ds_write_b32 v104, v45
	ds_write_b32 v106, v46
	ds_write_b32 v107, v47
	ds_write_b32 v108, v48
	ds_write_b32 v109, v49
	ds_write_b32 v111, v50
	ds_write_b32 v112, v51
	ds_write_b32 v113, v52
	ds_write_b32 v114, v53
	ds_write_b32 v116, v54
	ds_write_b32 v117, v55
	ds_write_b32 v118, v56
	ds_write_b32 v119, v57
	ds_write_b32 v121, v58
	ds_write_b32 v122, v59
	ds_write_b32 v123, v60
	ds_write_b32 v124, v61
	ds_write_b32 v126, v62
	ds_write_b32 v127, v63
	ds_write_b32 v128, v64
	ds_write_b32 v129, v65
	ds_write_b32 v131, v22
	ds_write_b32 v132, v23
	ds_write_b32 v133, v24
	ds_write_b32 v134, v25
	ds_write_b32 v136, v18
	ds_write_b32 v137, v19
	ds_write_b32 v138, v20
	ds_write_b32 v139, v21
	ds_write_b32 v141, v14
	ds_write_b32 v142, v15
	ds_write_b32 v143, v16
	ds_write_b32 v144, v17
	ds_write_b32 v146, v10
	ds_write_b32 v147, v11
	ds_write_b32 v148, v12
	ds_write_b32 v149, v13
	s_waitcnt lgkmcnt(0)
	s_add_i32 s26, s19, 0xfffffe00
	s_cmpk_gt_i32 s26, 0xfff
	s_cbranch_scc1 .LBB0_1364
	s_ashr_i32 s0, s19, 31
	s_lshr_b32 s0, s0, 23
	s_add_i32 s0, s19, s0
	s_ashr_i32 s0, s0, 9
	s_add_i32 s10, s0, 16
	s_ashr_i32 s11, s10, 31
	s_mov_b64 s[16:17], 0x32400000
	s_cmpk_lt_i32 s26, 0xfa01
	s_mov_b64 s[14:15], s[10:11]
	s_cbranch_scc1 .LBB0_1363
	s_cmp_gt_u32 s10, 21
	s_cbranch_scc0 .LBB0_1369
	s_add_i32 s14, s0, -6
	s_mov_b32 s15, s1
	s_mov_b64 s[16:17], 0x36400000
	s_cbranch_execnz .LBB0_1363
	s_branch .LBB0_1370

.LBB0_1370:
	s_mov_b64 s[16:17], 0x30c00000
	s_branch .LBB0_1363
.Lcv0_exit:
	s_waitcnt lgkmcnt(0)
	s_barrier
.LBB0_1371:
	s_mov_b32 s7, s89
	s_mov_b32 s6, s88
	s_waitcnt vmcnt(0)
	s_barrier
	s_and_saveexec_b64 s[4:5], s[82:83]
	s_cbranch_execz .LBB0_1415
	s_add_i32 s0, 0, 0x21000
	s_waitcnt vmcnt(0)
	v_mov_b32_e32 v1, s0
	s_waitcnt vmcnt(0) expcnt(0) lgkmcnt(0)
	ds_read_b32 v4, v1
	s_add_i32 s0, 0, 0x21004
	v_mov_b32_e32 v1, s0
	ds_read_b32 v2, v1
	s_waitcnt lgkmcnt(1)
	v_cmp_ne_u32_e32 vcc, 0, v4
	s_cbranch_vccnz .LBB0_1386
	v_readlane_b32 s8, v233, 32
	v_readlane_b32 s9, v233, 33
	s_load_dword s2, s[8:9], 0x14
	s_load_dwordx2 s[0:1], s[8:9], 0x4
	s_mov_b32 s25, 1
	s_waitcnt lgkmcnt(0)
	v_mov_b64_e32 v[2:3], s[6:7]
	s_lshr_b32 s8, s2, 16
	s_and_b32 s2, s2, 0xffff
	s_cmp_lg_u32 s2, 0
	s_cselect_b64 s[2:3], -1, 0
	s_cmp_lg_u64 s[2:3], 0
	s_addc_u32 s0, s0, 0
	s_cmp_lg_u32 s8, 0
	s_cselect_b64 s[2:3], -1, 0
	s_cmp_lg_u64 s[2:3], 0
	s_mul_i32 s24, s0, s90
	s_addc_u32 s0, s1, 0
	s_add_u32 s2, s6, 0x1000
	s_addc_u32 s3, s7, 0
	s_add_u32 s8, s6, 0x1100
	s_addc_u32 s9, s7, 0
	s_add_u32 s10, s6, 0x1200
	s_addc_u32 s11, s7, 0
	s_add_u32 s12, s6, 0x1300
	s_addc_u32 s13, s7, 0
	s_mul_i32 s24, s24, s0
	s_mov_b64 s[0:1], 0
	v_mov_b64_e32 v[4:5], s[2:3]
	v_mov_b64_e32 v[6:7], s[8:9]
	v_mov_b64_e32 v[8:9], s[10:11]
	v_mov_b64_e32 v[10:11], s[12:13]
	s_branch .LBB0_1376

.Lcv1_idle:
	s_lshr_b32 s25, s78, 1
	s_and_b32 s0, s8, 1
	s_add_i32 s25, s25, s0
	s_lshr_b32 s0, s8, 2
	s_lshl_b32 s0, s0, 1
	s_add_i32 s25, s25, s0
	s_cmpk_gt_i32 s25, 0x11ff
	s_cbranch_scc1 .Lcv1_exit
	s_ashr_i32 s0, s25, 31
	s_lshr_b32 s0, s0, 23
	s_add_i32 s0, s25, s0
	s_ashr_i32 s0, s0, 9
	s_add_i32 s12, s0, 16
	s_ashr_i32 s13, s12, 31
	s_mov_b64 s[14:15], 0x32400000
	s_cmpk_lt_i32 s25, 0xfe01
	s_mov_b64 s[6:7], s[12:13]
	s_cbranch_scc1 .LBB0_3680
	s_cmp_gt_u32 s12, 21
	s_mov_b32 s1, 0
	s_cbranch_scc0 .LBB0_3678
	s_add_i32 s6, s0, -6
	s_mov_b32 s7, s1
	s_mov_b64 s[14:15], 0x36400000
	s_cbranch_execz .LBB0_3679
	s_branch .LBB0_3680

.LBB0_3680:
	v_readlane_b32 s2, v232, 49
	v_readlane_b32 s3, v232, 50
	s_ashr_i32 s3, s2, 31
	s_lshl_b64 s[2:3], s[2:3], 27
	s_add_u32 s9, s64, s2
	s_addc_u32 s10, s65, s3
	s_add_u32 s11, s66, s2
	s_addc_u32 s24, s67, s3
	s_lshl_b32 s0, s0, 9
	s_sub_i32 s0, s25, s0
	s_cmpk_gt_i32 s0, 0xff
	s_cselect_b64 s[16:17], -1, 0
	s_and_b64 s[2:3], s[16:17], exec
	s_cselect_b32 s2, 0xff00, 0
	s_add_i32 s0, s2, s0
	s_sext_i32_i16 s2, s0
	s_bfe_u32 s2, s2, 0x5001a
	s_add_i32 s2, s0, s2
	s_sext_i32_i16 s3, s2
	s_and_b32 s2, s2, 0xffe0
	s_ashr_i32 s26, s3, 5
	s_sub_i32 s0, s0, s2
	s_lshl_b32 s18, s26, 6
	s_and_b64 s[2:3], s[16:17], exec
	s_sext_i32_i16 s19, s0
	s_cselect_b32 s0, s24, s10
	s_cselect_b32 s20, s11, s9
	s_lshl_b64 s[2:3], s[12:13], 22
	s_add_u32 s20, s20, s2
	s_addc_u32 s21, s0, s3
	s_lshl_b32 s12, s19, 6
	v_lshrrev_b32_e32 v70, 4, v1
	v_or_b32_e32 v2, s12, v70
	v_or_b32_e32 v4, 60, v2
	v_ashrrev_i32_e32 v5, 31, v4
	v_or_b32_e32 v6, 56, v2
	v_lshlrev_b64 v[4:5], 11, v[4:5]
	s_ashr_i32 s19, s18, 31
	v_lshlrev_b32_e32 v69, 2, v1
	v_ashrrev_i32_e32 v7, 31, v6
	v_lshl_add_u64 v[4:5], s[20:21], 0, v[4:5]
	s_lshl_b64 s[22:23], s[18:19], 2
	v_and_b32_e32 v68, 60, v69
	v_lshlrev_b64 v[6:7], 11, v[6:7]
	v_lshl_add_u64 v[4:5], v[4:5], 0, s[22:23]
	v_mov_b32_e32 v67, 0
	v_lshlrev_b32_e32 v66, 2, v68
	v_lshl_add_u64 v[6:7], s[20:21], 0, v[6:7]
	v_lshl_add_u64 v[4:5], v[4:5], 0, v[66:67]
	v_lshl_add_u64 v[6:7], v[6:7], 0, s[22:23]
	v_lshl_add_u64 v[6:7], v[6:7], 0, v[66:67]
	global_load_dwordx4 v[10:13], v[4:5], off nt
	global_load_dwordx4 v[14:17], v[6:7], off nt
	v_or_b32_e32 v4, 52, v2
	v_ashrrev_i32_e32 v5, 31, v4
	v_or_b32_e32 v6, 48, v2
	v_lshlrev_b64 v[4:5], 11, v[4:5]
	v_ashrrev_i32_e32 v7, 31, v6
	v_lshl_add_u64 v[4:5], s[20:21], 0, v[4:5]
	v_lshlrev_b64 v[6:7], 11, v[6:7]
	v_lshl_add_u64 v[4:5], v[4:5], 0, s[22:23]
	v_lshl_add_u64 v[6:7], s[20:21], 0, v[6:7]
	v_lshl_add_u64 v[4:5], v[4:5], 0, v[66:67]
	v_lshl_add_u64 v[6:7], v[6:7], 0, s[22:23]
	v_lshl_add_u64 v[6:7], v[6:7], 0, v[66:67]
	global_load_dwordx4 v[18:21], v[4:5], off nt
	global_load_dwordx4 v[22:25], v[6:7], off nt
	v_or_b32_e32 v4, 44, v2
	v_ashrrev_i32_e32 v5, 31, v4
	v_or_b32_e32 v6, 40, v2
	v_lshlrev_b64 v[4:5], 11, v[4:5]
	v_ashrrev_i32_e32 v7, 31, v6
	v_lshl_add_u64 v[4:5], s[20:21], 0, v[4:5]
	v_lshlrev_b64 v[6:7], 11, v[6:7]
	v_lshl_add_u64 v[4:5], v[4:5], 0, s[22:23]
	v_lshl_add_u64 v[6:7], s[20:21], 0, v[6:7]
	v_lshl_add_u64 v[4:5], v[4:5], 0, v[66:67]
	v_lshl_add_u64 v[6:7], v[6:7], 0, s[22:23]
	v_lshl_add_u64 v[6:7], v[6:7], 0, v[66:67]
	global_load_dwordx4 v[62:65], v[4:5], off nt
	global_load_dwordx4 v[58:61], v[6:7], off nt
	v_or_b32_e32 v4, 36, v2
	v_ashrrev_i32_e32 v5, 31, v4
	v_or_b32_e32 v6, 32, v2
	v_lshlrev_b64 v[4:5], 11, v[4:5]
	v_ashrrev_i32_e32 v7, 31, v6
	v_lshl_add_u64 v[4:5], s[20:21], 0, v[4:5]
	v_lshlrev_b64 v[6:7], 11, v[6:7]
	v_lshl_add_u64 v[4:5], v[4:5], 0, s[22:23]
	v_lshl_add_u64 v[6:7], s[20:21], 0, v[6:7]
	v_lshl_add_u64 v[4:5], v[4:5], 0, v[66:67]
	v_lshl_add_u64 v[6:7], v[6:7], 0, s[22:23]
	v_lshl_add_u64 v[6:7], v[6:7], 0, v[66:67]
	global_load_dwordx4 v[54:57], v[4:5], off nt
	global_load_dwordx4 v[50:53], v[6:7], off nt
	v_or_b32_e32 v4, 28, v2
	v_ashrrev_i32_e32 v5, 31, v4
	v_or_b32_e32 v6, 24, v2
	v_lshlrev_b64 v[4:5], 11, v[4:5]
	v_ashrrev_i32_e32 v7, 31, v6
	v_lshl_add_u64 v[4:5], s[20:21], 0, v[4:5]
	v_lshlrev_b64 v[6:7], 11, v[6:7]
	v_lshl_add_u64 v[4:5], v[4:5], 0, s[22:23]
	v_lshl_add_u64 v[6:7], s[20:21], 0, v[6:7]
	v_lshl_add_u64 v[4:5], v[4:5], 0, v[66:67]
	v_lshl_add_u64 v[6:7], v[6:7], 0, s[22:23]
	v_lshl_add_u64 v[6:7], v[6:7], 0, v[66:67]
	global_load_dwordx4 v[46:49], v[4:5], off nt
	global_load_dwordx4 v[42:45], v[6:7], off nt
	v_or_b32_e32 v4, 20, v2
	v_ashrrev_i32_e32 v5, 31, v4
	v_or_b32_e32 v6, 16, v2
	v_lshlrev_b64 v[4:5], 11, v[4:5]
	v_ashrrev_i32_e32 v7, 31, v6
	v_lshl_add_u64 v[4:5], s[20:21], 0, v[4:5]
	v_lshlrev_b64 v[6:7], 11, v[6:7]
	v_lshl_add_u64 v[4:5], v[4:5], 0, s[22:23]
	v_lshl_add_u64 v[6:7], s[20:21], 0, v[6:7]
	v_lshl_add_u64 v[4:5], v[4:5], 0, v[66:67]
	v_lshl_add_u64 v[6:7], v[6:7], 0, s[22:23]
	v_lshl_add_u64 v[6:7], v[6:7], 0, v[66:67]
	global_load_dwordx4 v[38:41], v[4:5], off nt
	global_load_dwordx4 v[34:37], v[6:7], off nt
	v_or_b32_e32 v4, 12, v2
	v_ashrrev_i32_e32 v5, 31, v4
	v_or_b32_e32 v6, 8, v2
	v_lshlrev_b64 v[4:5], 11, v[4:5]
	v_ashrrev_i32_e32 v7, 31, v6
	v_lshl_add_u64 v[4:5], s[20:21], 0, v[4:5]
	v_lshlrev_b64 v[6:7], 11, v[6:7]
	v_lshl_add_u64 v[4:5], v[4:5], 0, s[22:23]
	v_lshl_add_u64 v[6:7], s[20:21], 0, v[6:7]
	v_lshl_add_u64 v[4:5], v[4:5], 0, v[66:67]
	v_lshl_add_u64 v[6:7], v[6:7], 0, s[22:23]
	v_lshl_add_u64 v[6:7], v[6:7], 0, v[66:67]
	global_load_dwordx4 v[30:33], v[4:5], off nt
	global_load_dwordx4 v[26:29], v[6:7], off nt
	v_or_b32_e32 v4, 4, v2
	v_ashrrev_i32_e32 v5, 31, v4
	v_ashrrev_i32_e32 v3, 31, v2
	s_lshl_b32 s0, s8, 14
	v_lshlrev_b64 v[4:5], 11, v[4:5]
	v_lshlrev_b64 v[2:3], 11, v[2:3]
	s_add_i32 s0, s0, 0
	v_lshl_add_u64 v[4:5], s[20:21], 0, v[4:5]
	v_lshl_add_u64 v[2:3], s[20:21], 0, v[2:3]
	v_lshl_add_u64 v[4:5], v[4:5], 0, s[22:23]
	v_lshl_add_u64 v[2:3], v[2:3], 0, s[22:23]
	s_waitcnt vmcnt(14)
	v_lshl_add_u32 v74, v70, 8, s0
	v_lshlrev_b32_e32 v71, 2, v70
	v_lshl_add_u64 v[4:5], v[4:5], 0, v[66:67]
	v_lshl_add_u64 v[2:3], v[2:3], 0, v[66:67]
	v_add3_u32 v71, v74, v71, v66
	v_bitop3_b32 v66, v68, v70, 1 bitop3:0x36
	v_lshl_add_u32 v72, v66, 2, v74
	v_bitop3_b32 v66, v68, v70, 2 bitop3:0x36
	v_lshl_add_u32 v73, v66, 2, v74
	v_bitop3_b32 v66, v68, v70, 3 bitop3:0x36
	v_or_b32_e32 v75, 4, v70
	v_lshl_add_u32 v74, v66, 2, v74
	v_bitop3_b32 v66, v70, v68, 4 bitop3:0x36
	v_lshl_add_u32 v79, v75, 8, s0
	v_lshl_add_u32 v76, v66, 2, v79
	v_bitop3_b32 v66, v68, v75, 1 bitop3:0x36
	v_lshl_add_u32 v77, v66, 2, v79
	v_bitop3_b32 v66, v68, v75, 2 bitop3:0x36
	v_lshl_add_u32 v78, v66, 2, v79
	v_bitop3_b32 v66, v68, v75, 3 bitop3:0x36
	v_or_b32_e32 v80, 8, v70
	v_lshl_add_u32 v79, v66, 2, v79
	v_bitop3_b32 v66, v70, v68, 8 bitop3:0x36
	v_lshl_add_u32 v84, v80, 8, s0
	v_lshl_add_u32 v81, v66, 2, v84
	v_bitop3_b32 v66, v68, v80, 1 bitop3:0x36
	v_lshl_add_u32 v82, v66, 2, v84
	v_bitop3_b32 v66, v68, v80, 2 bitop3:0x36
	global_load_dwordx4 v[6:9], v[4:5], off nt
	s_nop 0
	global_load_dwordx4 v[2:5], v[2:3], off nt
	v_lshl_add_u32 v83, v66, 2, v84
	v_bitop3_b32 v66, v68, v80, 3 bitop3:0x36
	v_or_b32_e32 v85, 12, v70
	v_lshl_add_u32 v84, v66, 2, v84
	v_bitop3_b32 v66, v70, v68, 12 bitop3:0x36
	v_lshl_add_u32 v89, v85, 8, s0
	v_lshl_add_u32 v86, v66, 2, v89
	v_bitop3_b32 v66, v68, v85, 1 bitop3:0x36
	v_lshl_add_u32 v87, v66, 2, v89
	v_bitop3_b32 v66, v68, v85, 2 bitop3:0x36
	v_lshl_add_u32 v88, v66, 2, v89
	v_bitop3_b32 v66, v68, v85, 3 bitop3:0x36
	v_or_b32_e32 v90, 16, v70
	v_lshl_add_u32 v89, v66, 2, v89
	v_bitop3_b32 v66, v70, v68, 16 bitop3:0x36
	v_lshl_add_u32 v94, v90, 8, s0
	v_lshl_add_u32 v91, v66, 2, v94
	v_bitop3_b32 v66, v68, v90, 1 bitop3:0x36
	v_lshl_add_u32 v92, v66, 2, v94
	v_bitop3_b32 v66, v68, v90, 2 bitop3:0x36
	v_lshl_add_u32 v93, v66, 2, v94
	v_bitop3_b32 v66, v68, v90, 3 bitop3:0x36
	v_or_b32_e32 v95, 20, v70
	v_lshl_add_u32 v94, v66, 2, v94
	v_bitop3_b32 v66, v70, v68, 20 bitop3:0x36
	v_lshl_add_u32 v99, v95, 8, s0
	v_lshl_add_u32 v96, v66, 2, v99
	v_bitop3_b32 v66, v68, v95, 1 bitop3:0x36
	v_lshl_add_u32 v97, v66, 2, v99
	v_bitop3_b32 v66, v68, v95, 2 bitop3:0x36
	v_lshl_add_u32 v98, v66, 2, v99
	v_bitop3_b32 v66, v68, v95, 3 bitop3:0x36
	v_or_b32_e32 v100, 24, v70
	v_lshl_add_u32 v99, v66, 2, v99
	v_bitop3_b32 v66, v70, v68, 24 bitop3:0x36
	v_lshl_add_u32 v104, v100, 8, s0
	v_lshl_add_u32 v101, v66, 2, v104
	v_bitop3_b32 v66, v68, v100, 1 bitop3:0x36
	v_lshl_add_u32 v102, v66, 2, v104
	v_bitop3_b32 v66, v68, v100, 2 bitop3:0x36
	v_lshl_add_u32 v103, v66, 2, v104
	v_bitop3_b32 v66, v68, v100, 3 bitop3:0x36
	v_or_b32_e32 v105, 28, v70
	v_lshl_add_u32 v104, v66, 2, v104
	v_bitop3_b32 v66, v70, v68, 28 bitop3:0x36
	v_lshl_add_u32 v109, v105, 8, s0
	v_lshl_add_u32 v106, v66, 2, v109
	v_bitop3_b32 v66, v68, v105, 1 bitop3:0x36
	v_lshl_add_u32 v107, v66, 2, v109
	v_bitop3_b32 v66, v68, v105, 2 bitop3:0x36
	v_lshl_add_u32 v108, v66, 2, v109
	v_bitop3_b32 v66, v68, v105, 3 bitop3:0x36
	v_or_b32_e32 v110, 32, v70
	v_lshl_add_u32 v109, v66, 2, v109
	v_bitop3_b32 v66, v70, v68, 32 bitop3:0x36
	v_lshl_add_u32 v114, v110, 8, s0
	v_lshl_add_u32 v111, v66, 2, v114
	v_bitop3_b32 v66, v68, v110, 1 bitop3:0x36
	v_lshl_add_u32 v112, v66, 2, v114
	v_bitop3_b32 v66, v68, v110, 2 bitop3:0x36
	v_lshl_add_u32 v113, v66, 2, v114
	v_bitop3_b32 v66, v68, v110, 3 bitop3:0x36
	v_or_b32_e32 v115, 36, v70
	v_lshl_add_u32 v114, v66, 2, v114
	v_bitop3_b32 v66, v70, v68, 36 bitop3:0x36
	v_lshl_add_u32 v119, v115, 8, s0
	v_lshl_add_u32 v116, v66, 2, v119
	v_bitop3_b32 v66, v68, v115, 1 bitop3:0x36
	v_lshl_add_u32 v117, v66, 2, v119
	v_bitop3_b32 v66, v68, v115, 2 bitop3:0x36
	v_lshl_add_u32 v118, v66, 2, v119
	v_bitop3_b32 v66, v68, v115, 3 bitop3:0x36
	v_or_b32_e32 v120, 40, v70
	v_lshl_add_u32 v119, v66, 2, v119
	v_bitop3_b32 v66, v70, v68, 40 bitop3:0x36
	v_lshl_add_u32 v124, v120, 8, s0
	v_lshl_add_u32 v121, v66, 2, v124
	v_bitop3_b32 v66, v68, v120, 1 bitop3:0x36
	v_lshl_add_u32 v122, v66, 2, v124
	v_bitop3_b32 v66, v68, v120, 2 bitop3:0x36
	v_lshl_add_u32 v123, v66, 2, v124
	v_bitop3_b32 v66, v68, v120, 3 bitop3:0x36
	v_or_b32_e32 v125, 44, v70
	v_lshl_add_u32 v124, v66, 2, v124
	v_bitop3_b32 v66, v70, v68, 44 bitop3:0x36
	v_lshl_add_u32 v129, v125, 8, s0
	v_lshl_add_u32 v126, v66, 2, v129
	v_bitop3_b32 v66, v68, v125, 1 bitop3:0x36
	v_lshl_add_u32 v127, v66, 2, v129
	v_bitop3_b32 v66, v68, v125, 2 bitop3:0x36
	v_lshl_add_u32 v128, v66, 2, v129
	v_bitop3_b32 v66, v68, v125, 3 bitop3:0x36
	v_or_b32_e32 v130, 48, v70
	v_lshl_add_u32 v129, v66, 2, v129
	v_bitop3_b32 v66, v70, v68, 48 bitop3:0x36
	v_lshl_add_u32 v134, v130, 8, s0
	v_lshl_add_u32 v131, v66, 2, v134
	v_bitop3_b32 v66, v68, v130, 1 bitop3:0x36
	v_lshl_add_u32 v132, v66, 2, v134
	v_bitop3_b32 v66, v68, v130, 2 bitop3:0x36
	v_lshl_add_u32 v133, v66, 2, v134
	v_bitop3_b32 v66, v68, v130, 3 bitop3:0x36
	v_or_b32_e32 v135, 52, v70
	v_lshl_add_u32 v134, v66, 2, v134
	v_bitop3_b32 v66, v70, v68, 52 bitop3:0x36
	v_lshl_add_u32 v139, v135, 8, s0
	v_lshl_add_u32 v136, v66, 2, v139
	v_bitop3_b32 v66, v68, v135, 1 bitop3:0x36
	v_lshl_add_u32 v137, v66, 2, v139
	v_bitop3_b32 v66, v68, v135, 2 bitop3:0x36
	v_lshl_add_u32 v138, v66, 2, v139
	v_bitop3_b32 v66, v68, v135, 3 bitop3:0x36
	v_or_b32_e32 v140, 56, v70
	v_lshl_add_u32 v139, v66, 2, v139
	v_bitop3_b32 v66, v70, v68, 56 bitop3:0x36
	v_lshl_add_u32 v144, v140, 8, s0
	v_lshl_add_u32 v141, v66, 2, v144
	v_bitop3_b32 v66, v68, v140, 1 bitop3:0x36
	v_lshl_add_u32 v142, v66, 2, v144
	v_bitop3_b32 v66, v68, v140, 2 bitop3:0x36
	v_lshl_add_u32 v143, v66, 2, v144
	v_bitop3_b32 v66, v68, v140, 3 bitop3:0x36
	v_or_b32_e32 v145, 60, v70
	v_lshl_add_u32 v144, v66, 2, v144
	v_bitop3_b32 v66, v70, v69, 60 bitop3:0x72
	v_lshl_add_u32 v69, v145, 8, s0
	v_lshl_add_u32 v146, v66, 2, v69
	v_bitop3_b32 v66, v68, v145, 1 bitop3:0x36
	v_lshl_add_u32 v147, v66, 2, v69
	v_bitop3_b32 v66, v68, v145, 2 bitop3:0x36
	v_lshl_add_u32 v148, v66, 2, v69
	v_bitop3_b32 v66, v68, v145, 3 bitop3:0x36
	v_lshl_add_u32 v149, v66, 2, v69
	v_lshlrev_b32_e32 v66, 3, v1
	v_lshrrev_b32_e32 v150, 3, v1
	v_and_b32_e32 v222, 56, v66
	v_lshl_add_u32 v69, v222, 8, s0
	v_lshlrev_b32_e32 v1, 2, v222
	v_lshlrev_b32_e32 v151, 2, v150
	v_add3_u32 v1, v69, v1, v151
	v_or_b32_e32 v151, 1, v222
	v_bitop3_b32 v152, v222, v150, 1 bitop3:0x36
	v_lshl_add_u32 v214, v151, 8, s0
	v_lshl_add_u32 v151, v152, 2, v214
	v_or_b32_e32 v152, 2, v222
	v_bitop3_b32 v153, v222, v150, 2 bitop3:0x36
	v_lshl_add_u32 v215, v152, 8, s0
	v_lshl_add_u32 v152, v153, 2, v215
	v_or_b32_e32 v153, 3, v222
	v_bitop3_b32 v154, v222, v150, 3 bitop3:0x36
	v_lshl_add_u32 v216, v153, 8, s0
	v_lshl_add_u32 v153, v154, 2, v216
	v_or_b32_e32 v154, 4, v222
	v_bitop3_b32 v155, v222, v150, 4 bitop3:0x36
	v_lshl_add_u32 v217, v154, 8, s0
	v_lshl_add_u32 v154, v155, 2, v217
	v_or_b32_e32 v155, 5, v222
	v_bitop3_b32 v156, v222, v150, 5 bitop3:0x36
	v_lshl_add_u32 v218, v155, 8, s0
	v_lshl_add_u32 v155, v156, 2, v218
	v_or_b32_e32 v156, 6, v222
	v_bitop3_b32 v157, v222, v150, 6 bitop3:0x36
	v_lshl_add_u32 v219, v156, 8, s0
	v_lshl_add_u32 v156, v157, 2, v219
	v_or_b32_e32 v157, 7, v222
	v_bitop3_b32 v158, v222, v150, 7 bitop3:0x36
	v_lshl_add_u32 v220, v157, 8, s0
	v_lshl_add_u32 v157, v158, 2, v220
	v_or_b32_e32 v158, 8, v150
	v_or_b32_e32 v167, 16, v150
	v_or_b32_e32 v176, 24, v150
	v_or_b32_e32 v185, 32, v150
	v_or_b32_e32 v194, 40, v150
	v_or_b32_e32 v203, 48, v150
	s_and_b32 s8, s18, 64
	v_bitop3_b32 v159, v66, v158, 56 bitop3:0x6c
	v_bitop3_b32 v168, v66, v167, 56 bitop3:0x6c
	v_bitop3_b32 v177, v66, v176, 56 bitop3:0x6c
	v_bitop3_b32 v186, v66, v185, 56 bitop3:0x6c
	v_bitop3_b32 v195, v66, v194, 56 bitop3:0x6c
	v_bitop3_b32 v204, v66, v203, 56 bitop3:0x6c
	v_or_b32_e32 v212, 56, v150
	v_bitop3_b32 v66, v66, v150, 56 bitop3:0x4e
	s_and_b64 s[2:3], s[16:17], exec
	v_bitop3_b32 v160, v222, v158, 1 bitop3:0x36
	v_bitop3_b32 v169, v222, v167, 1 bitop3:0x36
	v_bitop3_b32 v178, v222, v176, 1 bitop3:0x36
	v_bitop3_b32 v187, v222, v185, 1 bitop3:0x36
	v_bitop3_b32 v196, v222, v194, 1 bitop3:0x36
	v_bitop3_b32 v205, v222, v203, 1 bitop3:0x36
	v_lshl_add_u32 v213, v66, 2, v69
	v_bitop3_b32 v66, v222, v212, 1 bitop3:0x36
	s_cselect_b32 s2, 0x80, 0
	s_lshl_b32 s3, s26, 7
	v_lshl_add_u32 v160, v160, 2, v214
	v_bitop3_b32 v161, v222, v158, 2 bitop3:0x36
	v_lshl_add_u32 v169, v169, 2, v214
	v_bitop3_b32 v170, v222, v167, 2 bitop3:0x36
	v_lshl_add_u32 v178, v178, 2, v214
	v_bitop3_b32 v179, v222, v176, 2 bitop3:0x36
	v_lshl_add_u32 v187, v187, 2, v214
	v_bitop3_b32 v188, v222, v185, 2 bitop3:0x36
	v_lshl_add_u32 v196, v196, 2, v214
	v_bitop3_b32 v197, v222, v194, 2 bitop3:0x36
	v_lshl_add_u32 v205, v205, 2, v214
	v_bitop3_b32 v206, v222, v203, 2 bitop3:0x36
	v_lshl_add_u32 v214, v66, 2, v214
	v_bitop3_b32 v66, v222, v212, 2 bitop3:0x36
	s_or_b32 s2, s8, s2
	s_and_b32 s3, s3, 0xffffff00
	v_lshl_add_u32 v161, v161, 2, v215
	v_bitop3_b32 v162, v222, v158, 3 bitop3:0x36
	v_lshl_add_u32 v170, v170, 2, v215
	v_bitop3_b32 v171, v222, v167, 3 bitop3:0x36
	v_lshl_add_u32 v179, v179, 2, v215
	v_bitop3_b32 v180, v222, v176, 3 bitop3:0x36
	v_lshl_add_u32 v188, v188, 2, v215
	v_bitop3_b32 v189, v222, v185, 3 bitop3:0x36
	v_lshl_add_u32 v197, v197, 2, v215
	v_bitop3_b32 v198, v222, v194, 3 bitop3:0x36
	v_lshl_add_u32 v206, v206, 2, v215
	v_bitop3_b32 v207, v222, v203, 3 bitop3:0x36
	v_lshl_add_u32 v215, v66, 2, v215
	v_bitop3_b32 v66, v222, v212, 3 bitop3:0x36
	s_or_b32 s8, s2, s3
	s_lshl_b64 s[2:3], s[6:7], 22
	v_lshl_add_u32 v162, v162, 2, v216
	v_bitop3_b32 v163, v222, v158, 4 bitop3:0x36
	v_lshl_add_u32 v171, v171, 2, v216
	v_bitop3_b32 v172, v222, v167, 4 bitop3:0x36
	v_lshl_add_u32 v180, v180, 2, v216
	v_bitop3_b32 v181, v222, v176, 4 bitop3:0x36
	v_lshl_add_u32 v189, v189, 2, v216
	v_bitop3_b32 v190, v222, v185, 4 bitop3:0x36
	v_lshl_add_u32 v198, v198, 2, v216
	v_bitop3_b32 v199, v222, v194, 4 bitop3:0x36
	v_lshl_add_u32 v207, v207, 2, v216
	v_bitop3_b32 v208, v222, v203, 4 bitop3:0x36
	v_lshl_add_u32 v216, v66, 2, v216
	v_bitop3_b32 v66, v222, v212, 4 bitop3:0x36
	s_add_u32 s2, s4, s2
	v_lshl_add_u32 v163, v163, 2, v217
	v_bitop3_b32 v164, v222, v158, 5 bitop3:0x36
	v_lshl_add_u32 v172, v172, 2, v217
	v_bitop3_b32 v173, v222, v167, 5 bitop3:0x36
	v_lshl_add_u32 v181, v181, 2, v217
	v_bitop3_b32 v182, v222, v176, 5 bitop3:0x36
	v_lshl_add_u32 v190, v190, 2, v217
	v_bitop3_b32 v191, v222, v185, 5 bitop3:0x36
	v_lshl_add_u32 v199, v199, 2, v217
	v_bitop3_b32 v200, v222, v194, 5 bitop3:0x36
	v_lshl_add_u32 v208, v208, 2, v217
	v_bitop3_b32 v209, v222, v203, 5 bitop3:0x36
	v_lshl_add_u32 v217, v66, 2, v217
	v_bitop3_b32 v66, v222, v212, 5 bitop3:0x36
	s_addc_u32 s3, s5, s3
	v_lshl_add_u32 v164, v164, 2, v218
	v_bitop3_b32 v165, v222, v158, 6 bitop3:0x36
	v_lshl_add_u32 v173, v173, 2, v218
	v_bitop3_b32 v174, v222, v167, 6 bitop3:0x36
	v_lshl_add_u32 v182, v182, 2, v218
	v_bitop3_b32 v183, v222, v176, 6 bitop3:0x36
	v_lshl_add_u32 v191, v191, 2, v218
	v_bitop3_b32 v192, v222, v185, 6 bitop3:0x36
	v_lshl_add_u32 v200, v200, 2, v218
	v_bitop3_b32 v201, v222, v194, 6 bitop3:0x36
	v_lshl_add_u32 v209, v209, 2, v218
	v_bitop3_b32 v210, v222, v203, 6 bitop3:0x36
	v_lshl_add_u32 v218, v66, 2, v218
	v_bitop3_b32 v66, v222, v212, 6 bitop3:0x36
	s_add_u32 s6, s2, s14
	v_lshl_add_u32 v165, v165, 2, v219
	v_bitop3_b32 v166, v222, v158, 7 bitop3:0x36
	v_lshl_add_u32 v174, v174, 2, v219
	v_bitop3_b32 v175, v222, v167, 7 bitop3:0x36
	v_lshl_add_u32 v183, v183, 2, v219
	v_bitop3_b32 v184, v222, v176, 7 bitop3:0x36
	v_lshl_add_u32 v192, v192, 2, v219
	v_bitop3_b32 v193, v222, v185, 7 bitop3:0x36
	v_lshl_add_u32 v201, v201, 2, v219
	v_bitop3_b32 v202, v222, v194, 7 bitop3:0x36
	v_lshl_add_u32 v210, v210, 2, v219
	v_bitop3_b32 v211, v222, v203, 7 bitop3:0x36
	v_lshl_add_u32 v219, v66, 2, v219
	v_bitop3_b32 v66, v222, v212, 7 bitop3:0x36
	s_mov_b32 s1, 0
	s_addc_u32 s7, s3, s15
	v_lshl_add_u32 v159, v159, 2, v69
	v_lshl_add_u32 v166, v166, 2, v220
	v_lshl_add_u32 v168, v168, 2, v69
	v_lshl_add_u32 v175, v175, 2, v220
	v_lshl_add_u32 v177, v177, 2, v69
	v_lshl_add_u32 v184, v184, 2, v220
	v_lshl_add_u32 v186, v186, 2, v69
	v_lshl_add_u32 v193, v193, 2, v220
	v_lshl_add_u32 v195, v195, 2, v69
	v_lshl_add_u32 v202, v202, 2, v220
	v_lshl_add_u32 v204, v204, 2, v69
	v_lshl_add_u32 v211, v211, 2, v220
	v_lshl_add_u32 v220, v66, 2, v220
	s_add_i32 s22, s25, 0x200
	v_lshlrev_b32_e32 v66, 2, v68
	s_movk_i32 s23, 0x7fff
	s_mov_b32 s25, 0xffff0000
	v_lshlrev_b32_e32 v68, 1, v222
	s_branch .LBB0_3683

.LBB0_3682:
	ds_read_b32 v69, v1
	ds_read_b32 v221, v151
	ds_read_b32 v223, v152
	ds_read_b32 v224, v153
	ds_read_b32 v225, v154
	ds_read_b32 v226, v155
	ds_read_b32 v227, v156
	ds_read_b32 v228, v157
	s_waitcnt lgkmcnt(7)
	v_bfe_u32 v222, v69, 16, 1
	v_add3_u32 v69, v69, v222, s23
	s_waitcnt lgkmcnt(6)
	v_bfe_u32 v222, v221, 16, 1
	v_lshrrev_b32_e32 v69, 16, v69
	v_add3_u32 v221, v221, v222, s23
	v_and_or_b32 v222, v221, s25, v69
	s_waitcnt lgkmcnt(5)
	v_bfe_u32 v69, v223, 16, 1
	v_add3_u32 v69, v223, v69, s23
	s_waitcnt lgkmcnt(4)
	v_bfe_u32 v221, v224, 16, 1
	v_lshrrev_b32_e32 v69, 16, v69
	v_add3_u32 v221, v224, v221, s23
	v_and_or_b32 v223, v221, s25, v69
	s_waitcnt lgkmcnt(3)
	v_bfe_u32 v69, v225, 16, 1
	v_add3_u32 v69, v225, v69, s23
	s_waitcnt lgkmcnt(2)
	v_bfe_u32 v221, v226, 16, 1
	v_lshrrev_b32_e32 v69, 16, v69
	v_add3_u32 v221, v226, v221, s23
	v_and_or_b32 v224, v221, s25, v69
	s_waitcnt lgkmcnt(1)
	v_bfe_u32 v69, v227, 16, 1
	v_add_u32_e32 v226, s8, v150
	v_add3_u32 v69, v227, v69, s23
	v_ashrrev_i32_e32 v227, 31, v226
	s_waitcnt lgkmcnt(0)
	v_bfe_u32 v221, v228, 16, 1
	v_lshlrev_b64 v[226:227], 12, v[226:227]
	s_ashr_i32 s13, s12, 31
	v_lshrrev_b32_e32 v69, 16, v69
	v_add3_u32 v221, v228, v221, s23
	v_lshl_add_u64 v[226:227], s[6:7], 0, v[226:227]
	s_lshl_b64 s[12:13], s[12:13], 1
	v_and_or_b32 v225, v221, s25, v69
	v_lshl_add_u64 v[226:227], v[226:227], 0, s[12:13]
	v_mov_b32_e32 v69, v67
	v_lshl_add_u64 v[226:227], v[226:227], 0, v[68:69]
	global_store_dwordx4 v[226:227], v[222:225], off nt
	ds_read_b32 v221, v159
	ds_read_b32 v222, v160
	ds_read_b32 v223, v161
	ds_read_b32 v224, v162
	ds_read_b32 v225, v163
	ds_read_b32 v226, v164
	ds_read_b32 v227, v165
	ds_read_b32 v228, v166
	s_waitcnt lgkmcnt(7)
	v_bfe_u32 v229, v221, 16, 1
	v_add3_u32 v221, v221, v229, s23
	s_waitcnt lgkmcnt(6)
	v_bfe_u32 v229, v222, 16, 1
	v_lshrrev_b32_e32 v221, 16, v221
	v_add3_u32 v222, v222, v229, s23
	v_and_or_b32 v222, v222, s25, v221
	s_waitcnt lgkmcnt(5)
	v_bfe_u32 v221, v223, 16, 1
	v_add3_u32 v221, v223, v221, s23
	s_waitcnt lgkmcnt(4)
	v_bfe_u32 v223, v224, 16, 1
	v_lshrrev_b32_e32 v221, 16, v221
	v_add3_u32 v223, v224, v223, s23
	v_and_or_b32 v223, v223, s25, v221
	s_waitcnt lgkmcnt(3)
	v_bfe_u32 v221, v225, 16, 1
	v_add3_u32 v221, v225, v221, s23
	s_waitcnt lgkmcnt(2)
	v_bfe_u32 v224, v226, 16, 1
	v_lshrrev_b32_e32 v221, 16, v221
	v_add3_u32 v224, v226, v224, s23
	v_and_or_b32 v224, v224, s25, v221
	s_waitcnt lgkmcnt(1)
	v_bfe_u32 v221, v227, 16, 1
	v_add_u32_e32 v226, s8, v158
	v_add3_u32 v221, v227, v221, s23
	v_ashrrev_i32_e32 v227, 31, v226
	v_lshlrev_b64 v[226:227], 12, v[226:227]
	s_waitcnt lgkmcnt(0)
	v_bfe_u32 v225, v228, 16, 1
	v_lshl_add_u64 v[226:227], s[6:7], 0, v[226:227]
	v_lshrrev_b32_e32 v221, 16, v221
	v_add3_u32 v225, v228, v225, s23
	v_lshl_add_u64 v[226:227], v[226:227], 0, s[12:13]
	v_and_or_b32 v225, v225, s25, v221
	v_lshl_add_u64 v[226:227], v[226:227], 0, v[68:69]
	global_store_dwordx4 v[226:227], v[222:225], off nt
	ds_read_b32 v221, v168
	ds_read_b32 v222, v169
	ds_read_b32 v223, v170
	ds_read_b32 v224, v171
	ds_read_b32 v225, v172
	ds_read_b32 v226, v173
	ds_read_b32 v227, v174
	ds_read_b32 v228, v175
	s_waitcnt lgkmcnt(7)
	v_bfe_u32 v229, v221, 16, 1
	v_add3_u32 v221, v221, v229, s23
	s_waitcnt lgkmcnt(6)
	v_bfe_u32 v229, v222, 16, 1
	v_lshrrev_b32_e32 v221, 16, v221
	v_add3_u32 v222, v222, v229, s23
	v_and_or_b32 v222, v222, s25, v221
	s_waitcnt lgkmcnt(5)
	v_bfe_u32 v221, v223, 16, 1
	v_add3_u32 v221, v223, v221, s23
	s_waitcnt lgkmcnt(4)
	v_bfe_u32 v223, v224, 16, 1
	v_lshrrev_b32_e32 v221, 16, v221
	v_add3_u32 v223, v224, v223, s23
	v_and_or_b32 v223, v223, s25, v221
	s_waitcnt lgkmcnt(3)
	v_bfe_u32 v221, v225, 16, 1
	v_add3_u32 v221, v225, v221, s23
	s_waitcnt lgkmcnt(2)
	v_bfe_u32 v224, v226, 16, 1
	v_lshrrev_b32_e32 v221, 16, v221
	v_add3_u32 v224, v226, v224, s23
	v_and_or_b32 v224, v224, s25, v221
	s_waitcnt lgkmcnt(1)
	v_bfe_u32 v221, v227, 16, 1
	v_add_u32_e32 v226, s8, v167
	v_add3_u32 v221, v227, v221, s23
	v_ashrrev_i32_e32 v227, 31, v226
	v_lshlrev_b64 v[226:227], 12, v[226:227]
	s_waitcnt lgkmcnt(0)
	v_bfe_u32 v225, v228, 16, 1
	v_lshl_add_u64 v[226:227], s[6:7], 0, v[226:227]
	v_lshrrev_b32_e32 v221, 16, v221
	v_add3_u32 v225, v228, v225, s23
	v_lshl_add_u64 v[226:227], v[226:227], 0, s[12:13]
	v_and_or_b32 v225, v225, s25, v221
	v_lshl_add_u64 v[226:227], v[226:227], 0, v[68:69]
	global_store_dwordx4 v[226:227], v[222:225], off nt
	ds_read_b32 v221, v177
	ds_read_b32 v222, v178
	ds_read_b32 v223, v179
	ds_read_b32 v224, v180
	ds_read_b32 v225, v181
	ds_read_b32 v226, v182
	ds_read_b32 v227, v183
	ds_read_b32 v228, v184
	s_waitcnt lgkmcnt(7)
	v_bfe_u32 v229, v221, 16, 1
	v_add3_u32 v221, v221, v229, s23
	s_waitcnt lgkmcnt(6)
	v_bfe_u32 v229, v222, 16, 1
	v_lshrrev_b32_e32 v221, 16, v221
	v_add3_u32 v222, v222, v229, s23
	v_and_or_b32 v222, v222, s25, v221
	s_waitcnt lgkmcnt(5)
	v_bfe_u32 v221, v223, 16, 1
	v_add3_u32 v221, v223, v221, s23
	s_waitcnt lgkmcnt(4)
	v_bfe_u32 v223, v224, 16, 1
	v_lshrrev_b32_e32 v221, 16, v221
	v_add3_u32 v223, v224, v223, s23
	v_and_or_b32 v223, v223, s25, v221
	s_waitcnt lgkmcnt(3)
	v_bfe_u32 v221, v225, 16, 1
	v_add3_u32 v221, v225, v221, s23
	s_waitcnt lgkmcnt(2)
	v_bfe_u32 v224, v226, 16, 1
	v_lshrrev_b32_e32 v221, 16, v221
	v_add3_u32 v224, v226, v224, s23
	v_and_or_b32 v224, v224, s25, v221
	s_waitcnt lgkmcnt(1)
	v_bfe_u32 v221, v227, 16, 1
	v_add_u32_e32 v226, s8, v176
	v_add3_u32 v221, v227, v221, s23
	v_ashrrev_i32_e32 v227, 31, v226
	v_lshlrev_b64 v[226:227], 12, v[226:227]
	s_waitcnt lgkmcnt(0)
	v_bfe_u32 v225, v228, 16, 1
	v_lshl_add_u64 v[226:227], s[6:7], 0, v[226:227]
	v_lshrrev_b32_e32 v221, 16, v221
	v_add3_u32 v225, v228, v225, s23
	v_lshl_add_u64 v[226:227], v[226:227], 0, s[12:13]
	v_and_or_b32 v225, v225, s25, v221
	v_lshl_add_u64 v[226:227], v[226:227], 0, v[68:69]
	global_store_dwordx4 v[226:227], v[222:225], off nt
	ds_read_b32 v221, v186
	ds_read_b32 v222, v187
	ds_read_b32 v223, v188
	ds_read_b32 v224, v189
	ds_read_b32 v225, v190
	ds_read_b32 v226, v191
	ds_read_b32 v227, v192
	ds_read_b32 v228, v193
	s_waitcnt lgkmcnt(7)
	v_bfe_u32 v229, v221, 16, 1
	v_add3_u32 v221, v221, v229, s23
	s_waitcnt lgkmcnt(6)
	v_bfe_u32 v229, v222, 16, 1
	v_lshrrev_b32_e32 v221, 16, v221
	v_add3_u32 v222, v222, v229, s23
	v_and_or_b32 v222, v222, s25, v221
	s_waitcnt lgkmcnt(5)
	v_bfe_u32 v221, v223, 16, 1
	v_add3_u32 v221, v223, v221, s23
	s_waitcnt lgkmcnt(4)
	v_bfe_u32 v223, v224, 16, 1
	v_lshrrev_b32_e32 v221, 16, v221
	v_add3_u32 v223, v224, v223, s23
	v_and_or_b32 v223, v223, s25, v221
	s_waitcnt lgkmcnt(3)
	v_bfe_u32 v221, v225, 16, 1
	v_add3_u32 v221, v225, v221, s23
	s_waitcnt lgkmcnt(2)
	v_bfe_u32 v224, v226, 16, 1
	v_lshrrev_b32_e32 v221, 16, v221
	v_add3_u32 v224, v226, v224, s23
	v_and_or_b32 v224, v224, s25, v221
	s_waitcnt lgkmcnt(1)
	v_bfe_u32 v221, v227, 16, 1
	v_add_u32_e32 v226, s8, v185
	v_add3_u32 v221, v227, v221, s23
	v_ashrrev_i32_e32 v227, 31, v226
	v_lshlrev_b64 v[226:227], 12, v[226:227]
	s_waitcnt lgkmcnt(0)
	v_bfe_u32 v225, v228, 16, 1
	v_lshl_add_u64 v[226:227], s[6:7], 0, v[226:227]
	v_lshrrev_b32_e32 v221, 16, v221
	v_add3_u32 v225, v228, v225, s23
	v_lshl_add_u64 v[226:227], v[226:227], 0, s[12:13]
	v_and_or_b32 v225, v225, s25, v221
	v_lshl_add_u64 v[226:227], v[226:227], 0, v[68:69]
	global_store_dwordx4 v[226:227], v[222:225], off nt
	ds_read_b32 v221, v195
	ds_read_b32 v222, v196
	ds_read_b32 v223, v197
	ds_read_b32 v224, v198
	ds_read_b32 v225, v199
	ds_read_b32 v226, v200
	ds_read_b32 v227, v201
	ds_read_b32 v228, v202
	s_waitcnt lgkmcnt(7)
	v_bfe_u32 v229, v221, 16, 1
	v_add3_u32 v221, v221, v229, s23
	s_waitcnt lgkmcnt(6)
	v_bfe_u32 v229, v222, 16, 1
	v_lshrrev_b32_e32 v221, 16, v221
	v_add3_u32 v222, v222, v229, s23
	v_and_or_b32 v222, v222, s25, v221
	s_waitcnt lgkmcnt(5)
	v_bfe_u32 v221, v223, 16, 1
	v_add3_u32 v221, v223, v221, s23
	s_waitcnt lgkmcnt(4)
	v_bfe_u32 v223, v224, 16, 1
	v_lshrrev_b32_e32 v221, 16, v221
	v_add3_u32 v223, v224, v223, s23
	v_and_or_b32 v223, v223, s25, v221
	s_waitcnt lgkmcnt(3)
	v_bfe_u32 v221, v225, 16, 1
	v_add3_u32 v221, v225, v221, s23
	s_waitcnt lgkmcnt(2)
	v_bfe_u32 v224, v226, 16, 1
	v_lshrrev_b32_e32 v221, 16, v221
	v_add3_u32 v224, v226, v224, s23
	v_and_or_b32 v224, v224, s25, v221
	s_waitcnt lgkmcnt(1)
	v_bfe_u32 v221, v227, 16, 1
	v_add_u32_e32 v226, s8, v194
	v_add3_u32 v221, v227, v221, s23
	v_ashrrev_i32_e32 v227, 31, v226
	v_lshlrev_b64 v[226:227], 12, v[226:227]
	s_waitcnt lgkmcnt(0)
	v_bfe_u32 v225, v228, 16, 1
	v_lshl_add_u64 v[226:227], s[6:7], 0, v[226:227]
	v_lshrrev_b32_e32 v221, 16, v221
	v_add3_u32 v225, v228, v225, s23
	v_lshl_add_u64 v[226:227], v[226:227], 0, s[12:13]
	v_and_or_b32 v225, v225, s25, v221
	v_lshl_add_u64 v[226:227], v[226:227], 0, v[68:69]
	global_store_dwordx4 v[226:227], v[222:225], off nt
	ds_read_b32 v221, v204
	ds_read_b32 v222, v205
	ds_read_b32 v223, v206
	ds_read_b32 v224, v207
	ds_read_b32 v225, v208
	ds_read_b32 v226, v209
	ds_read_b32 v227, v210
	ds_read_b32 v228, v211
	s_waitcnt lgkmcnt(7)
	v_bfe_u32 v229, v221, 16, 1
	v_add3_u32 v221, v221, v229, s23
	s_waitcnt lgkmcnt(6)
	v_bfe_u32 v229, v222, 16, 1
	v_lshrrev_b32_e32 v221, 16, v221
	v_add3_u32 v222, v222, v229, s23
	v_and_or_b32 v222, v222, s25, v221
	s_waitcnt lgkmcnt(5)
	v_bfe_u32 v221, v223, 16, 1
	v_add3_u32 v221, v223, v221, s23
	s_waitcnt lgkmcnt(4)
	v_bfe_u32 v223, v224, 16, 1
	v_lshrrev_b32_e32 v221, 16, v221
	v_add3_u32 v223, v224, v223, s23
	v_and_or_b32 v223, v223, s25, v221
	s_waitcnt lgkmcnt(3)
	v_bfe_u32 v221, v225, 16, 1
	v_add3_u32 v221, v225, v221, s23
	s_waitcnt lgkmcnt(2)
	v_bfe_u32 v224, v226, 16, 1
	v_lshrrev_b32_e32 v221, 16, v221
	v_add3_u32 v224, v226, v224, s23
	v_and_or_b32 v224, v224, s25, v221
	s_waitcnt lgkmcnt(1)
	v_bfe_u32 v221, v227, 16, 1
	v_add_u32_e32 v226, s8, v203
	v_add3_u32 v221, v227, v221, s23
	v_ashrrev_i32_e32 v227, 31, v226
	v_lshlrev_b64 v[226:227], 12, v[226:227]
	s_waitcnt lgkmcnt(0)
	v_bfe_u32 v225, v228, 16, 1
	v_lshl_add_u64 v[226:227], s[6:7], 0, v[226:227]
	v_lshrrev_b32_e32 v221, 16, v221
	v_add3_u32 v225, v228, v225, s23
	v_lshl_add_u64 v[226:227], v[226:227], 0, s[12:13]
	v_and_or_b32 v225, v225, s25, v221
	v_lshl_add_u64 v[226:227], v[226:227], 0, v[68:69]
	global_store_dwordx4 v[226:227], v[222:225], off nt
	ds_read_b32 v221, v213
	ds_read_b32 v222, v214
	ds_read_b32 v223, v215
	ds_read_b32 v224, v216
	ds_read_b32 v225, v217
	ds_read_b32 v226, v218
	ds_read_b32 v227, v219
	ds_read_b32 v228, v220
	s_waitcnt lgkmcnt(7)
	v_bfe_u32 v229, v221, 16, 1
	v_add3_u32 v221, v221, v229, s23
	s_waitcnt lgkmcnt(6)
	v_bfe_u32 v229, v222, 16, 1
	v_lshrrev_b32_e32 v221, 16, v221
	v_add3_u32 v222, v222, v229, s23
	v_and_or_b32 v222, v222, s25, v221
	s_waitcnt lgkmcnt(5)
	v_bfe_u32 v221, v223, 16, 1
	v_add3_u32 v221, v223, v221, s23
	s_waitcnt lgkmcnt(4)
	v_bfe_u32 v223, v224, 16, 1
	v_lshrrev_b32_e32 v221, 16, v221
	v_add3_u32 v223, v224, v223, s23
	v_and_or_b32 v223, v223, s25, v221
	s_waitcnt lgkmcnt(3)
	v_bfe_u32 v221, v225, 16, 1
	v_add3_u32 v221, v225, v221, s23
	s_waitcnt lgkmcnt(2)
	v_bfe_u32 v224, v226, 16, 1
	v_lshrrev_b32_e32 v221, 16, v221
	v_add3_u32 v224, v226, v224, s23
	v_and_or_b32 v224, v224, s25, v221
	s_waitcnt lgkmcnt(1)
	v_bfe_u32 v221, v227, 16, 1
	v_add_u32_e32 v226, s8, v212
	v_add3_u32 v221, v227, v221, s23
	v_ashrrev_i32_e32 v227, 31, v226
	v_lshlrev_b64 v[226:227], 12, v[226:227]
	s_waitcnt lgkmcnt(0)
	v_bfe_u32 v225, v228, 16, 1
	v_lshl_add_u64 v[226:227], s[6:7], 0, v[226:227]
	v_lshrrev_b32_e32 v221, 16, v221
	v_add3_u32 v225, v228, v225, s23
	v_lshl_add_u64 v[226:227], v[226:227], 0, s[12:13]
	v_and_or_b32 v225, v225, s25, v221
	v_lshl_add_u64 v[226:227], v[226:227], 0, v[68:69]
	global_store_dwordx4 v[226:227], v[222:225], off nt
	s_waitcnt lgkmcnt(0)
	s_addk_i32 s22, 0x200
	s_cmpk_gt_i32 s26, 0xfff
	s_mov_b64 s[6:7], s[14:15]
	s_mov_b32 s12, s0
	s_mov_b32 s8, s16
	s_cbranch_scc1 .Lcv1_exit
.LBB0_3683:
	s_waitcnt vmcnt(0)
	ds_write_b32 v71, v2
	ds_write_b32 v72, v3
	ds_write_b32 v73, v4
	ds_write_b32 v74, v5
	ds_write_b32 v76, v6
	ds_write_b32 v77, v7
	ds_write_b32 v78, v8
	ds_write_b32 v79, v9
	ds_write_b32 v81, v26
	ds_write_b32 v82, v27
	ds_write_b32 v83, v28
	ds_write_b32 v84, v29
	ds_write_b32 v86, v30
	ds_write_b32 v87, v31
	ds_write_b32 v88, v32
	ds_write_b32 v89, v33
	ds_write_b32 v91, v34
	ds_write_b32 v92, v35
	ds_write_b32 v93, v36
	ds_write_b32 v94, v37
	ds_write_b32 v96, v38
	ds_write_b32 v97, v39
	ds_write_b32 v98, v40
	ds_write_b32 v99, v41
	ds_write_b32 v101, v42
	ds_write_b32 v102, v43
	ds_write_b32 v103, v44
	ds_write_b32 v104, v45
	ds_write_b32 v106, v46
	ds_write_b32 v107, v47
	ds_write_b32 v108, v48
	ds_write_b32 v109, v49
	ds_write_b32 v111, v50
	ds_write_b32 v112, v51
	ds_write_b32 v113, v52
	ds_write_b32 v114, v53
	ds_write_b32 v116, v54
	ds_write_b32 v117, v55
	ds_write_b32 v118, v56
	ds_write_b32 v119, v57
	ds_write_b32 v121, v58
	ds_write_b32 v122, v59
	ds_write_b32 v123, v60
	ds_write_b32 v124, v61
	ds_write_b32 v126, v62
	ds_write_b32 v127, v63
	ds_write_b32 v128, v64
	ds_write_b32 v129, v65
	ds_write_b32 v131, v22
	ds_write_b32 v132, v23
	ds_write_b32 v133, v24
	ds_write_b32 v134, v25
	ds_write_b32 v136, v18
	ds_write_b32 v137, v19
	ds_write_b32 v138, v20
	ds_write_b32 v139, v21
	ds_write_b32 v141, v14
	ds_write_b32 v142, v15
	ds_write_b32 v143, v16
	ds_write_b32 v144, v17
	ds_write_b32 v146, v10
	ds_write_b32 v147, v11
	ds_write_b32 v148, v12
	ds_write_b32 v149, v13
	s_waitcnt lgkmcnt(0)
	s_add_i32 s26, s22, 0xfffffe00
	s_cmpk_gt_i32 s26, 0xfff
	s_cbranch_scc1 .LBB0_3682
	s_ashr_i32 s0, s22, 31
	s_lshr_b32 s0, s0, 23
	s_add_i32 s0, s22, s0
	s_ashr_i32 s0, s0, 9
	s_add_i32 s14, s0, 16
	s_ashr_i32 s15, s14, 31
	s_mov_b64 s[20:21], 0x32400000
	s_cmpk_lt_i32 s26, 0xfa01
	s_mov_b64 s[18:19], s[14:15]
	s_cbranch_scc1 .LBB0_3681
	s_cmp_gt_u32 s14, 21
	s_cbranch_scc0 .LBB0_3687
	s_add_i32 s18, s0, -6
	s_mov_b32 s19, s1
	s_mov_b64 s[20:21], 0x36400000
	s_cbranch_execnz .LBB0_3681
	s_branch .LBB0_3688

.LBB0_3688:
	s_mov_b64 s[20:21], 0x30c00000
	s_branch .LBB0_3681
.Lcv1_exit:
	s_waitcnt lgkmcnt(0)
	s_barrier
.LBB0_3689:
	s_mov_b32 s40, s82
	s_mov_b32 s41, s83
	s_waitcnt vmcnt(0)
	s_barrier
	s_and_saveexec_b64 s[4:5], s[84:85]
	s_cbranch_execz .LBB0_3733
	s_add_i32 s0, 0, 0x21000
	s_waitcnt vmcnt(0)
	v_mov_b32_e32 v1, s0
	s_waitcnt vmcnt(0) expcnt(0) lgkmcnt(0)
	ds_read_b32 v4, v1
	s_add_i32 s0, 0, 0x21004
	v_mov_b32_e32 v1, s0
	ds_read_b32 v2, v1
	s_waitcnt lgkmcnt(1)
	v_cmp_ne_u32_e32 vcc, 0, v4
	s_cbranch_vccnz .LBB0_3704
	v_readlane_b32 s6, v233, 32
	v_readlane_b32 s7, v233, 33
	s_load_dword s2, s[6:7], 0x14
	s_load_dwordx2 s[0:1], s[6:7], 0x4
	s_mov_b32 s9, 1
	s_waitcnt lgkmcnt(0)
	v_mov_b64_e32 v[2:3], s[40:41]
	s_lshr_b32 s6, s2, 16
	s_and_b32 s2, s2, 0xffff
	s_cmp_lg_u32 s2, 0
	s_cselect_b64 s[2:3], -1, 0
	s_cmp_lg_u64 s[2:3], 0
	s_addc_u32 s0, s0, 0
	s_cmp_lg_u32 s6, 0
	s_cselect_b64 s[2:3], -1, 0
	s_cmp_lg_u64 s[2:3], 0
	s_mul_i32 s8, s0, s76
	s_addc_u32 s0, s1, 0
	s_add_u32 s2, s40, 0x1000
	s_addc_u32 s3, s41, 0
	s_add_u32 s6, s40, 0x1100
	s_addc_u32 s7, s41, 0
	s_add_u32 s10, s40, 0x1200
	s_addc_u32 s11, s41, 0
	s_add_u32 s12, s40, 0x1300
	s_addc_u32 s13, s41, 0
	s_mul_i32 s8, s8, s0
	s_mov_b64 s[0:1], 0
	v_mov_b64_e32 v[4:5], s[2:3]
	v_mov_b64_e32 v[6:7], s[6:7]
	v_mov_b64_e32 v[8:9], s[10:11]
	v_mov_b64_e32 v[10:11], s[12:13]
	s_branch .LBB0_3694
